# waves 4-7 sleep ~320 cycles (s_sleep 5) after their per-tile barrier before starting the softmax, so waves 0-3 get their tile DMA and first P.V MFMAs issued unimpeded
# speedup vs baseline: 1.0125x; 1.0020x over previous
.LBB0_517:
	s_or_b64 exec, exec, s[4:5]
	s_lshr_b32 s3, s2, 1
	s_mul_i32 s3, s15, s3
	v_readlane_b32 s4, v255, 16
	s_add_i32 s33, s4, s3
	s_lshl_b32 s3, s33, 7
	s_and_b32 s6, s3, 0xfffff000
	s_lshl_b32 s3, s33, 8
	s_ashr_i32 s82, s33, 3
	s_and_b32 s3, s3, 0x700
	s_and_b32 s2, s2, 1
	s_and_b32 s69, s82, 3
	s_xor_b32 s4, s3, 0xf00
	s_cmp_eq_u32 s2, 0
	s_mov_b32 s2, s6
	s_cselect_b32 s84, s4, s3
	v_writelane_b32 v255, s2, 46
	s_ashr_i32 s7, s6, 31
	s_lshl_b64 s[66:67], s[6:7], 11
	v_writelane_b32 v255, s3, 47
	v_mov_b32_e32 v0, v165
	v_readlane_b32 s2, v255, 25
	s_add_u32 s2, s2, s66
	v_readlane_b32 s3, v255, 26
	s_addc_u32 s3, s3, s67
	s_lshl_b32 s4, s69, 8
	s_add_u32 s6, s2, s4
	s_addc_u32 s7, s3, 0
	s_add_u32 s3, s6, 0x400
	v_writelane_b32 v255, s4, 48
	s_addc_u32 s68, s7, 0
	s_ashr_i32 s83, s82, 31
	s_lshl_b64 s[4:5], s[82:83], 14
	v_readlane_b32 s2, v255, 17
	s_add_u32 s8, s2, s4
	v_readlane_b32 s2, v255, 18
	s_addc_u32 s9, s2, s5
	s_lshl_b32 s4, s82, 6
	s_ashr_i32 s5, s4, 31
	s_lshl_b64 s[4:5], s[4:5], 2
	v_readlane_b32 s2, v255, 21
	s_add_u32 s4, s2, s4
	v_readlane_b32 s2, v255, 22
	s_addc_u32 s5, s2, s5
	v_mov_b32_e32 v3, v161
	v_readfirstlane_b32 s2, v0
	s_ashr_i32 s10, s2, 6
	s_lshl_b32 s12, s10, 5
	s_mov_b32 s2, s12
	v_and_b32_e32 v39, 63, v0
	v_writelane_b32 v255, s2, 49
	s_add_i32 s94, s12, s84
	v_lshlrev_b32_e32 v2, 2, v39
	v_writelane_b32 v255, s3, 50
	s_lshl_b32 s2, s10, 11
	v_lshl_add_u64 v[4:5], s[4:5], 0, v[2:3]
	v_readlane_b32 s11, v255, 28
	s_lshl_b32 s4, s10, 12
	s_ashr_i32 s95, s94, 31
	s_lshl_b32 s78, s10, 3
	flat_load_dword v3, v[4:5]
	s_add_i32 s2, s2, s11
	s_add_i32 s81, s4, s79
	s_lshl_b64 s[12:13], s[94:95], 2
	v_and_b32_e32 v175, 31, v0
	s_add_u32 s4, s8, s12
	v_writelane_b32 v255, s12, 51
	s_addc_u32 s5, s9, s13
	v_lshlrev_b32_e32 v160, 2, v175
	v_lshl_add_u64 v[4:5], s[4:5], 0, v[160:161]
	flat_load_dword v178, v[4:5]
	v_bfe_u32 v4, v0, 4, 2
	v_bitop3_b32 v6, v4, v0, 15 bitop3:0x78
	v_add_u32_e32 v2, s89, v2
	v_writelane_b32 v255, s13, 52
	v_bfe_u32 v176, v0, 5, 1
	v_lshlrev_b32_e32 v6, 4, v6
	v_or_b32_e32 v4, s78, v4
	v_and_b32_e32 v5, 15, v0
	v_lshlrev_b32_e32 v1, 2, v176
	s_mulk_i32 s10, 0x1c00
	v_lshl_or_b32 v170, v4, 11, v6
	v_or_b32_e32 v4, 4, v4
	v_readlane_b32 s4, v255, 33
	v_lshlrev_b32_e32 v40, 4, v39
	v_sub_u32_e32 v7, v175, v1
	v_bitop3_b32 v5, v4, v5, 7 bitop3:0x6c
	v_lshlrev_b32_e32 v4, 11, v4
	s_add_i32 s4, s4, s10
	v_add_u32_e32 v180, s94, v7
	v_lshl_or_b32 v172, v5, 4, v4
	v_add_u32_e32 v181, s4, v40
	v_lshlrev_b32_e32 v174, 4, v176
	s_waitcnt vmcnt(0) lgkmcnt(0)
	ds_write_b32 v2, v3
	s_waitcnt vmcnt(0)
	ds_write_b128 v181, v[128:131]
	ds_write_b128 v181, v[132:135] offset:1024
	ds_write_b128 v181, v[136:139] offset:2048
	ds_write_b128 v181, v[140:143] offset:3072
	ds_write_b128 v181, v[144:147] offset:4096
	ds_write_b128 v181, v[148:151] offset:5120
	ds_write_b128 v181, v[152:155] offset:6144
	s_add_u32 s4, s6, 0x20400
	s_addc_u32 s5, s7, 0
	v_mov_b32_e32 v171, v161
	v_lshl_add_u64 v[2:3], s[4:5], 0, v[170:171]
	s_add_i32 s96, s2, 0x4000
	s_mov_b32 s6, m0
	s_mov_b32 m0, s96
	s_nop 0
	global_load_lds_dwordx4 v[2:3], off
	s_mov_b32 m0, s6
	v_mov_b32_e32 v173, v161
	v_lshl_add_u64 v[2:3], s[4:5], 0, v[172:173]
	s_add_i32 s97, s2, 0x4400
	s_mov_b32 s4, m0
	s_mov_b32 m0, s97
	s_nop 0
	global_load_lds_dwordx4 v[2:3], off
	s_mov_b32 m0, s4
	s_waitcnt lgkmcnt(0)
	s_barrier
	v_lshlrev_b32_e32 v2, 4, v0
	s_movk_i32 s4, 0x70
	v_lshlrev_b32_e32 v34, 8, v175
	v_and_b32_e32 v3, 0x70, v2
	v_bitop3_b32 v35, v174, v2, s4 bitop3:0x78
	s_movk_i32 s4, 0x60
	v_add_u32_e32 v4, s11, v34
	v_bitop3_b32 v36, v174, v3, 32 bitop3:0x36
	v_bitop3_b32 v37, v174, v3, 64 bitop3:0x36
	v_bitop3_b32 v38, v174, v3, s4 bitop3:0x36
	v_add_u32_e32 v182, v35, v4
	v_add_u32_e32 v183, v36, v4
	v_add_u32_e32 v184, v37, v4
	v_add_u32_e32 v185, v38, v4
	ds_read_b128 v[2:5], v182 offset:0
	ds_read_b128 v[6:9], v182 offset:0x2000
	ds_read_b128 v[10:13], v181 offset:0
	ds_read_b128 v[42:45], v183 offset:0
	ds_read_b128 v[46:49], v183 offset:0x2000
	ds_read_b128 v[50:53], v181 offset:0x400
	s_waitcnt lgkmcnt(3)
	s_nop 0
	v_mfma_f32_32x32x16_bf16 v[18:33], v[2:5], v[10:13], 0
	v_mfma_f32_32x32x16_bf16 v[2:17], v[6:9], v[10:13], 0
	ds_read_b128 v[54:57], v184 offset:0
	ds_read_b128 v[58:61], v184 offset:0x2000
	ds_read_b128 v[62:65], v181 offset:0x800
	s_waitcnt lgkmcnt(3)
	v_mfma_f32_32x32x16_bf16 v[18:33], v[42:45], v[50:53], v[18:33]
	v_mfma_f32_32x32x16_bf16 v[2:17], v[46:49], v[50:53], v[2:17]
	ds_read_b128 v[42:45], v185 offset:0
	ds_read_b128 v[46:49], v185 offset:0x2000
	ds_read_b128 v[50:53], v181 offset:0xc00
	s_waitcnt lgkmcnt(3)
	v_mfma_f32_32x32x16_bf16 v[18:33], v[54:57], v[62:65], v[18:33]
	v_mfma_f32_32x32x16_bf16 v[2:17], v[58:61], v[62:65], v[2:17]
	ds_read_b128 v[54:57], v182 offset:0x80
	ds_read_b128 v[58:61], v182 offset:0x2080
	ds_read_b128 v[62:65], v181 offset:0x1000
	s_waitcnt lgkmcnt(3)
	v_mfma_f32_32x32x16_bf16 v[18:33], v[42:45], v[50:53], v[18:33]
	v_mfma_f32_32x32x16_bf16 v[2:17], v[46:49], v[50:53], v[2:17]
	ds_read_b128 v[42:45], v183 offset:0x80
	ds_read_b128 v[46:49], v183 offset:0x2080
	ds_read_b128 v[50:53], v181 offset:0x1400
	s_waitcnt lgkmcnt(3)
	v_mfma_f32_32x32x16_bf16 v[18:33], v[54:57], v[62:65], v[18:33]
	v_mfma_f32_32x32x16_bf16 v[2:17], v[58:61], v[62:65], v[2:17]
	ds_read_b128 v[54:57], v184 offset:0x80
	ds_read_b128 v[58:61], v184 offset:0x2080
	ds_read_b128 v[62:65], v181 offset:0x1800
	s_waitcnt lgkmcnt(3)
	v_mfma_f32_32x32x16_bf16 v[18:33], v[42:45], v[50:53], v[18:33]
	v_mfma_f32_32x32x16_bf16 v[2:17], v[46:49], v[50:53], v[2:17]
	ds_read_b128 v[42:45], v185 offset:0x80
	ds_read_b128 v[46:49], v185 offset:0x2080
	s_waitcnt lgkmcnt(2)
	v_mfma_f32_32x32x16_bf16 v[18:33], v[54:57], v[62:65], v[18:33]
	v_mfma_f32_32x32x16_bf16 v[2:17], v[58:61], v[62:65], v[2:17]
	s_waitcnt lgkmcnt(0)
	v_mfma_f32_32x32x16_bf16 v[18:33], v[42:45], v[166:169], v[18:33]
	v_mfma_f32_32x32x16_bf16 v[2:17], v[46:49], v[166:169], v[2:17]
	s_bitcmp0_b32 s100, 8
	s_cbranch_scc1 .Lstg_a1
	s_waitcnt vmcnt(0)
	s_waitcnt lgkmcnt(0)
	s_barrier
	s_sleep 5

.LBB0_520:
	ds_read_b64_tr_b16 v[144:145], v177 offset:0
	ds_read_b64_tr_b16 v[146:147], v177 offset:0x1000
	ds_read_b64_tr_b16 v[148:149], v177 offset:0x2000
	ds_read_b64_tr_b16 v[150:151], v177 offset:0x3000
	ds_read_b64_tr_b16 v[152:153], v177 offset:0x4000
	ds_read_b64_tr_b16 v[154:155], v177 offset:0x5000
	ds_read_b64_tr_b16 v[156:157], v177 offset:0x6000
	ds_read_b64_tr_b16 v[158:159], v177 offset:0x7000
	s_waitcnt lgkmcnt(6)
	s_nop 0
	v_mfma_f32_32x32x16_bf16 v[112:127], v[144:147], v[128:131], v[112:127]
	ds_read_b64_tr_b16 v[198:199], v177 offset:0x200
	ds_read_b64_tr_b16 v[200:201], v177 offset:0x1200
	s_waitcnt lgkmcnt(6)
	v_mfma_f32_32x32x16_bf16 v[112:127], v[148:151], v[132:135], v[112:127]
	ds_read_b64_tr_b16 v[202:203], v177 offset:0x2200
	ds_read_b64_tr_b16 v[204:205], v177 offset:0x3200
	s_waitcnt lgkmcnt(6)
	v_mfma_f32_32x32x16_bf16 v[112:127], v[152:155], v[136:139], v[112:127]
	ds_read_b64_tr_b16 v[206:207], v177 offset:0x4200
	ds_read_b64_tr_b16 v[208:209], v177 offset:0x5200
	s_waitcnt lgkmcnt(6)
	v_mfma_f32_32x32x16_bf16 v[112:127], v[156:159], v[140:143], v[112:127]
	ds_read_b64_tr_b16 v[210:211], v177 offset:0x6200
	ds_read_b64_tr_b16 v[212:213], v177 offset:0x7200
	s_waitcnt lgkmcnt(6)
	v_mfma_f32_32x32x16_bf16 v[0:15], v[198:201], v[128:131], v[0:15]
	ds_read_b64_tr_b16 v[144:145], v177 offset:0x400
	ds_read_b64_tr_b16 v[146:147], v177 offset:0x1400
	s_waitcnt lgkmcnt(6)
	v_mfma_f32_32x32x16_bf16 v[0:15], v[202:205], v[132:135], v[0:15]
	ds_read_b64_tr_b16 v[148:149], v177 offset:0x2400
	ds_read_b64_tr_b16 v[150:151], v177 offset:0x3400
	s_waitcnt lgkmcnt(6)
	v_mfma_f32_32x32x16_bf16 v[0:15], v[206:209], v[136:139], v[0:15]
	ds_read_b64_tr_b16 v[152:153], v177 offset:0x4400
	ds_read_b64_tr_b16 v[154:155], v177 offset:0x5400
	s_waitcnt lgkmcnt(6)
	v_mfma_f32_32x32x16_bf16 v[0:15], v[210:213], v[140:143], v[0:15]
	ds_read_b64_tr_b16 v[156:157], v177 offset:0x6400
	ds_read_b64_tr_b16 v[158:159], v177 offset:0x7400
	s_waitcnt lgkmcnt(6)
	v_mfma_f32_32x32x16_bf16 v[16:31], v[144:147], v[128:131], v[16:31]
	ds_read_b64_tr_b16 v[198:199], v177 offset:0x600
	ds_read_b64_tr_b16 v[200:201], v177 offset:0x1600
	s_waitcnt lgkmcnt(6)
	v_mfma_f32_32x32x16_bf16 v[16:31], v[148:151], v[132:135], v[16:31]
	ds_read_b64_tr_b16 v[202:203], v177 offset:0x2600
	ds_read_b64_tr_b16 v[204:205], v177 offset:0x3600
	s_waitcnt lgkmcnt(6)
	v_mfma_f32_32x32x16_bf16 v[16:31], v[152:155], v[136:139], v[16:31]
	ds_read_b64_tr_b16 v[206:207], v177 offset:0x4600
	ds_read_b64_tr_b16 v[208:209], v177 offset:0x5600
	s_waitcnt lgkmcnt(6)
	v_mfma_f32_32x32x16_bf16 v[16:31], v[156:159], v[140:143], v[16:31]
	ds_read_b64_tr_b16 v[210:211], v177 offset:0x6600
	ds_read_b64_tr_b16 v[212:213], v177 offset:0x7600
	s_waitcnt lgkmcnt(6)
	v_mfma_f32_32x32x16_bf16 v[32:47], v[198:201], v[128:131], v[32:47]
	ds_read_b64_tr_b16 v[144:145], v177 offset:0x800
	ds_read_b64_tr_b16 v[146:147], v177 offset:0x1800
	s_waitcnt lgkmcnt(6)
	v_mfma_f32_32x32x16_bf16 v[32:47], v[202:205], v[132:135], v[32:47]
	ds_read_b64_tr_b16 v[148:149], v177 offset:0x2800
	ds_read_b64_tr_b16 v[150:151], v177 offset:0x3800
	s_waitcnt lgkmcnt(6)
	v_mfma_f32_32x32x16_bf16 v[32:47], v[206:209], v[136:139], v[32:47]
	ds_read_b64_tr_b16 v[152:153], v177 offset:0x4800
	ds_read_b64_tr_b16 v[154:155], v177 offset:0x5800
	s_waitcnt lgkmcnt(6)
	v_mfma_f32_32x32x16_bf16 v[32:47], v[210:213], v[140:143], v[32:47]
	ds_read_b64_tr_b16 v[156:157], v177 offset:0x6800
	ds_read_b64_tr_b16 v[158:159], v177 offset:0x7800
	s_waitcnt lgkmcnt(6)
	v_mfma_f32_32x32x16_bf16 v[48:63], v[144:147], v[128:131], v[48:63]
	ds_read_b64_tr_b16 v[198:199], v177 offset:0xa00
	ds_read_b64_tr_b16 v[200:201], v177 offset:0x1a00
	s_waitcnt lgkmcnt(6)
	v_mfma_f32_32x32x16_bf16 v[48:63], v[148:151], v[132:135], v[48:63]
	ds_read_b64_tr_b16 v[202:203], v177 offset:0x2a00
	ds_read_b64_tr_b16 v[204:205], v177 offset:0x3a00
	s_waitcnt lgkmcnt(6)
	v_mfma_f32_32x32x16_bf16 v[48:63], v[152:155], v[136:139], v[48:63]
	ds_read_b64_tr_b16 v[206:207], v177 offset:0x4a00
	ds_read_b64_tr_b16 v[208:209], v177 offset:0x5a00
	s_waitcnt lgkmcnt(6)
	v_mfma_f32_32x32x16_bf16 v[48:63], v[156:159], v[140:143], v[48:63]
	ds_read_b64_tr_b16 v[210:211], v177 offset:0x6a00
	ds_read_b64_tr_b16 v[212:213], v177 offset:0x7a00
	s_waitcnt lgkmcnt(6)
	v_mfma_f32_32x32x16_bf16 v[64:79], v[198:201], v[128:131], v[64:79]
	ds_read_b64_tr_b16 v[144:145], v177 offset:0xc00
	ds_read_b64_tr_b16 v[146:147], v177 offset:0x1c00
	s_waitcnt lgkmcnt(6)
	v_mfma_f32_32x32x16_bf16 v[64:79], v[202:205], v[132:135], v[64:79]
	ds_read_b64_tr_b16 v[148:149], v177 offset:0x2c00
	ds_read_b64_tr_b16 v[150:151], v177 offset:0x3c00
	s_waitcnt lgkmcnt(6)
	v_mfma_f32_32x32x16_bf16 v[64:79], v[206:209], v[136:139], v[64:79]
	ds_read_b64_tr_b16 v[152:153], v177 offset:0x4c00
	ds_read_b64_tr_b16 v[154:155], v177 offset:0x5c00
	s_waitcnt lgkmcnt(6)
	v_mfma_f32_32x32x16_bf16 v[64:79], v[210:213], v[140:143], v[64:79]
	ds_read_b64_tr_b16 v[156:157], v177 offset:0x6c00
	ds_read_b64_tr_b16 v[158:159], v177 offset:0x7c00
	s_waitcnt lgkmcnt(6)
	v_mfma_f32_32x32x16_bf16 v[80:95], v[144:147], v[128:131], v[80:95]
	ds_read_b64_tr_b16 v[198:199], v177 offset:0xe00
	ds_read_b64_tr_b16 v[200:201], v177 offset:0x1e00
	s_waitcnt lgkmcnt(6)
	v_mfma_f32_32x32x16_bf16 v[80:95], v[148:151], v[132:135], v[80:95]
	ds_read_b64_tr_b16 v[202:203], v177 offset:0x2e00
	ds_read_b64_tr_b16 v[204:205], v177 offset:0x3e00
	s_waitcnt lgkmcnt(6)
	v_mfma_f32_32x32x16_bf16 v[80:95], v[152:155], v[136:139], v[80:95]
	ds_read_b64_tr_b16 v[206:207], v177 offset:0x4e00
	ds_read_b64_tr_b16 v[208:209], v177 offset:0x5e00
	s_waitcnt lgkmcnt(6)
	v_mfma_f32_32x32x16_bf16 v[80:95], v[156:159], v[140:143], v[80:95]
	ds_read_b64_tr_b16 v[210:211], v177 offset:0x6e00
	ds_read_b64_tr_b16 v[212:213], v177 offset:0x7e00
	s_waitcnt lgkmcnt(6)
	v_mfma_f32_32x32x16_bf16 v[96:111], v[198:201], v[128:131], v[96:111]
	s_waitcnt lgkmcnt(4)
	v_mfma_f32_32x32x16_bf16 v[96:111], v[202:205], v[132:135], v[96:111]
	s_waitcnt lgkmcnt(2)
	v_mfma_f32_32x32x16_bf16 v[96:111], v[206:209], v[136:139], v[96:111]
	s_waitcnt lgkmcnt(0)
	v_mfma_f32_32x32x16_bf16 v[96:111], v[210:213], v[140:143], v[96:111]
	ds_read_b128 v[128:131], v189 offset:0
	ds_read_b128 v[132:135], v189 offset:0x2000
	ds_read_b128 v[136:139], v181 offset:0
	ds_read_b128 v[198:201], v188 offset:0
	ds_read_b128 v[202:205], v188 offset:0x2000
	ds_read_b128 v[206:209], v181 offset:0x400
	s_waitcnt lgkmcnt(3)
	s_nop 0
	v_mfma_f32_32x32x16_bf16 v[144:159], v[128:131], v[136:139], 0
	v_mfma_f32_32x32x16_bf16 v[128:143], v[132:135], v[136:139], 0
	ds_read_b128 v[210:213], v187 offset:0
	ds_read_b128 v[214:217], v187 offset:0x2000
	ds_read_b128 v[218:221], v181 offset:0x800
	s_waitcnt lgkmcnt(3)
	v_mfma_f32_32x32x16_bf16 v[144:159], v[198:201], v[206:209], v[144:159]
	v_mfma_f32_32x32x16_bf16 v[128:143], v[202:205], v[206:209], v[128:143]
	ds_read_b128 v[198:201], v186 offset:0
	ds_read_b128 v[202:205], v186 offset:0x2000
	ds_read_b128 v[206:209], v181 offset:0xc00
	s_waitcnt lgkmcnt(3)
	v_mfma_f32_32x32x16_bf16 v[144:159], v[210:213], v[218:221], v[144:159]
	v_mfma_f32_32x32x16_bf16 v[128:143], v[214:217], v[218:221], v[128:143]
	ds_read_b128 v[210:213], v189 offset:0x80
	ds_read_b128 v[214:217], v189 offset:0x2080
	ds_read_b128 v[218:221], v181 offset:0x1000
	s_waitcnt lgkmcnt(3)
	v_mfma_f32_32x32x16_bf16 v[144:159], v[198:201], v[206:209], v[144:159]
	v_mfma_f32_32x32x16_bf16 v[128:143], v[202:205], v[206:209], v[128:143]
	ds_read_b128 v[198:201], v188 offset:0x80
	ds_read_b128 v[202:205], v188 offset:0x2080
	ds_read_b128 v[206:209], v181 offset:0x1400
	s_waitcnt lgkmcnt(3)
	v_mfma_f32_32x32x16_bf16 v[144:159], v[210:213], v[218:221], v[144:159]
	v_mfma_f32_32x32x16_bf16 v[128:143], v[214:217], v[218:221], v[128:143]
	ds_read_b128 v[210:213], v187 offset:0x80
	ds_read_b128 v[214:217], v187 offset:0x2080
	ds_read_b128 v[218:221], v181 offset:0x1800
	s_waitcnt lgkmcnt(3)
	v_mfma_f32_32x32x16_bf16 v[144:159], v[198:201], v[206:209], v[144:159]
	v_mfma_f32_32x32x16_bf16 v[128:143], v[202:205], v[206:209], v[128:143]
	ds_read_b128 v[198:201], v186 offset:0x80
	ds_read_b128 v[202:205], v186 offset:0x2080
	s_waitcnt lgkmcnt(2)
	v_mfma_f32_32x32x16_bf16 v[144:159], v[210:213], v[218:221], v[144:159]
	v_mfma_f32_32x32x16_bf16 v[128:143], v[214:217], v[218:221], v[128:143]
	s_waitcnt lgkmcnt(0)
	v_mfma_f32_32x32x16_bf16 v[144:159], v[198:201], v[166:169], v[144:159]
	v_mfma_f32_32x32x16_bf16 v[128:143], v[202:205], v[166:169], v[128:143]
	s_bitcmp0_b32 s100, 8
	s_cbranch_scc1 .Lstg_a2
	s_waitcnt vmcnt(0)
	s_waitcnt lgkmcnt(0)
	s_barrier
	s_sleep 5

.LBB0_526:
	s_add_u32 s33, s72, s84
	s_addc_u32 s92, s73, s90
	s_add_u32 s4, s33, 0x2dd40800
	s_addc_u32 s5, s92, 0
	s_mov_b32 m0, s81
	s_nop 0
	global_load_lds_dwordx4 v162, s[4:5]
	s_add_i32 m0, s78, 0xffffff80
	s_nop 0
	global_load_lds_dwordx4 v162, s[4:5] offset:128
	s_add_i32 m0, s69, 0xffffff00
	s_nop 0
	global_load_lds_dwordx4 v162, s[4:5] offset:256
	s_add_i32 m0, s68, 0xfffffe80
	s_nop 0
	global_load_lds_dwordx4 v162, s[4:5] offset:384
	ds_read_b64_tr_b16 v[144:145], v177 offset:0x8000
	ds_read_b64_tr_b16 v[146:147], v177 offset:0x9000
	ds_read_b64_tr_b16 v[148:149], v177 offset:0xa000
	ds_read_b64_tr_b16 v[150:151], v177 offset:0xb000
	ds_read_b64_tr_b16 v[152:153], v177 offset:0xc000
	ds_read_b64_tr_b16 v[154:155], v177 offset:0xd000
	ds_read_b64_tr_b16 v[156:157], v177 offset:0xe000
	ds_read_b64_tr_b16 v[158:159], v177 offset:0xf000
	s_waitcnt lgkmcnt(6)
	s_nop 1
	v_mfma_f32_32x32x16_bf16 v[112:127], v[144:147], v[128:131], v[112:127]
	ds_read_b64_tr_b16 v[236:237], v177 offset:0x8200
	ds_read_b64_tr_b16 v[238:239], v177 offset:0x9200
	s_waitcnt lgkmcnt(6)
	v_mfma_f32_32x32x16_bf16 v[112:127], v[148:151], v[132:135], v[112:127]
	ds_read_b64_tr_b16 v[240:241], v177 offset:0xa200
	ds_read_b64_tr_b16 v[242:243], v177 offset:0xb200
	s_waitcnt lgkmcnt(6)
	v_mfma_f32_32x32x16_bf16 v[112:127], v[152:155], v[136:139], v[112:127]
	ds_read_b64_tr_b16 v[244:245], v177 offset:0xc200
	ds_read_b64_tr_b16 v[246:247], v177 offset:0xd200
	s_waitcnt lgkmcnt(6)
	v_mfma_f32_32x32x16_bf16 v[112:127], v[156:159], v[140:143], v[112:127]
	ds_read_b64_tr_b16 v[248:249], v177 offset:0xe200
	ds_read_b64_tr_b16 v[250:251], v177 offset:0xf200
	s_waitcnt lgkmcnt(6)
	v_mfma_f32_32x32x16_bf16 v[0:15], v[236:239], v[128:131], v[0:15]
	ds_read_b64_tr_b16 v[144:145], v177 offset:0x8400
	ds_read_b64_tr_b16 v[146:147], v177 offset:0x9400
	s_waitcnt lgkmcnt(6)
	v_mfma_f32_32x32x16_bf16 v[0:15], v[240:243], v[132:135], v[0:15]
	ds_read_b64_tr_b16 v[148:149], v177 offset:0xa400
	ds_read_b64_tr_b16 v[150:151], v177 offset:0xb400
	s_waitcnt lgkmcnt(6)
	v_mfma_f32_32x32x16_bf16 v[0:15], v[244:247], v[136:139], v[0:15]
	ds_read_b64_tr_b16 v[152:153], v177 offset:0xc400
	ds_read_b64_tr_b16 v[154:155], v177 offset:0xd400
	s_waitcnt lgkmcnt(6)
	v_mfma_f32_32x32x16_bf16 v[0:15], v[248:251], v[140:143], v[0:15]
	ds_read_b64_tr_b16 v[156:157], v177 offset:0xe400
	ds_read_b64_tr_b16 v[158:159], v177 offset:0xf400
	s_waitcnt lgkmcnt(6)
	v_mfma_f32_32x32x16_bf16 v[16:31], v[144:147], v[128:131], v[16:31]
	ds_read_b64_tr_b16 v[236:237], v177 offset:0x8600
	ds_read_b64_tr_b16 v[238:239], v177 offset:0x9600
	s_waitcnt lgkmcnt(6)
	v_mfma_f32_32x32x16_bf16 v[16:31], v[148:151], v[132:135], v[16:31]
	ds_read_b64_tr_b16 v[240:241], v177 offset:0xa600
	ds_read_b64_tr_b16 v[242:243], v177 offset:0xb600
	s_waitcnt lgkmcnt(6)
	v_mfma_f32_32x32x16_bf16 v[16:31], v[152:155], v[136:139], v[16:31]
	ds_read_b64_tr_b16 v[244:245], v177 offset:0xc600
	ds_read_b64_tr_b16 v[246:247], v177 offset:0xd600
	s_waitcnt lgkmcnt(6)
	v_mfma_f32_32x32x16_bf16 v[16:31], v[156:159], v[140:143], v[16:31]
	ds_read_b64_tr_b16 v[248:249], v177 offset:0xe600
	ds_read_b64_tr_b16 v[250:251], v177 offset:0xf600
	s_waitcnt lgkmcnt(6)
	v_mfma_f32_32x32x16_bf16 v[32:47], v[236:239], v[128:131], v[32:47]
	ds_read_b64_tr_b16 v[144:145], v177 offset:0x8800
	ds_read_b64_tr_b16 v[146:147], v177 offset:0x9800
	s_waitcnt lgkmcnt(6)
	v_mfma_f32_32x32x16_bf16 v[32:47], v[240:243], v[132:135], v[32:47]
	ds_read_b64_tr_b16 v[148:149], v177 offset:0xa800
	ds_read_b64_tr_b16 v[150:151], v177 offset:0xb800
	s_waitcnt lgkmcnt(6)
	v_mfma_f32_32x32x16_bf16 v[32:47], v[244:247], v[136:139], v[32:47]
	ds_read_b64_tr_b16 v[152:153], v177 offset:0xc800
	ds_read_b64_tr_b16 v[154:155], v177 offset:0xd800
	s_waitcnt lgkmcnt(6)
	v_mfma_f32_32x32x16_bf16 v[32:47], v[248:251], v[140:143], v[32:47]
	ds_read_b64_tr_b16 v[156:157], v177 offset:0xe800
	ds_read_b64_tr_b16 v[158:159], v177 offset:0xf800
	s_waitcnt lgkmcnt(6)
	v_mfma_f32_32x32x16_bf16 v[48:63], v[144:147], v[128:131], v[48:63]
	ds_read_b64_tr_b16 v[236:237], v177 offset:0x8a00
	ds_read_b64_tr_b16 v[238:239], v177 offset:0x9a00
	s_waitcnt lgkmcnt(6)
	v_mfma_f32_32x32x16_bf16 v[48:63], v[148:151], v[132:135], v[48:63]
	ds_read_b64_tr_b16 v[240:241], v177 offset:0xaa00
	ds_read_b64_tr_b16 v[242:243], v177 offset:0xba00
	s_waitcnt lgkmcnt(6)
	v_mfma_f32_32x32x16_bf16 v[48:63], v[152:155], v[136:139], v[48:63]
	ds_read_b64_tr_b16 v[244:245], v177 offset:0xca00
	ds_read_b64_tr_b16 v[246:247], v177 offset:0xda00
	s_waitcnt lgkmcnt(6)
	v_mfma_f32_32x32x16_bf16 v[48:63], v[156:159], v[140:143], v[48:63]
	ds_read_b64_tr_b16 v[248:249], v177 offset:0xea00
	ds_read_b64_tr_b16 v[250:251], v177 offset:0xfa00
	s_waitcnt lgkmcnt(6)
	v_mfma_f32_32x32x16_bf16 v[64:79], v[236:239], v[128:131], v[64:79]
	ds_read_b64_tr_b16 v[144:145], v177 offset:0x8c00
	ds_read_b64_tr_b16 v[146:147], v177 offset:0x9c00
	s_waitcnt lgkmcnt(6)
	v_mfma_f32_32x32x16_bf16 v[64:79], v[240:243], v[132:135], v[64:79]
	ds_read_b64_tr_b16 v[148:149], v177 offset:0xac00
	ds_read_b64_tr_b16 v[150:151], v177 offset:0xbc00
	s_waitcnt lgkmcnt(6)
	v_mfma_f32_32x32x16_bf16 v[64:79], v[244:247], v[136:139], v[64:79]
	ds_read_b64_tr_b16 v[152:153], v177 offset:0xcc00
	ds_read_b64_tr_b16 v[154:155], v177 offset:0xdc00
	s_waitcnt lgkmcnt(6)
	v_mfma_f32_32x32x16_bf16 v[64:79], v[248:251], v[140:143], v[64:79]
	ds_read_b64_tr_b16 v[156:157], v177 offset:0xec00
	ds_read_b64_tr_b16 v[158:159], v177 offset:0xfc00
	s_waitcnt lgkmcnt(6)
	v_mfma_f32_32x32x16_bf16 v[80:95], v[144:147], v[128:131], v[80:95]
	ds_read_b64_tr_b16 v[236:237], v177 offset:0x8e00
	ds_read_b64_tr_b16 v[238:239], v177 offset:0x9e00
	s_waitcnt lgkmcnt(6)
	v_mfma_f32_32x32x16_bf16 v[80:95], v[148:151], v[132:135], v[80:95]
	ds_read_b64_tr_b16 v[240:241], v177 offset:0xae00
	ds_read_b64_tr_b16 v[242:243], v177 offset:0xbe00
	s_waitcnt lgkmcnt(6)
	v_mfma_f32_32x32x16_bf16 v[80:95], v[152:155], v[136:139], v[80:95]
	ds_read_b64_tr_b16 v[244:245], v177 offset:0xce00
	ds_read_b64_tr_b16 v[246:247], v177 offset:0xde00
	s_waitcnt lgkmcnt(6)
	v_mfma_f32_32x32x16_bf16 v[80:95], v[156:159], v[140:143], v[80:95]
	ds_read_b64_tr_b16 v[248:249], v177 offset:0xee00
	ds_read_b64_tr_b16 v[250:251], v177 offset:0xfe00
	s_waitcnt lgkmcnt(6)
	v_mfma_f32_32x32x16_bf16 v[96:111], v[236:239], v[128:131], v[96:111]
	s_waitcnt lgkmcnt(4)
	v_mfma_f32_32x32x16_bf16 v[96:111], v[240:243], v[132:135], v[96:111]
	s_waitcnt lgkmcnt(2)
	v_mfma_f32_32x32x16_bf16 v[96:111], v[244:247], v[136:139], v[96:111]
	s_waitcnt lgkmcnt(0)
	v_mfma_f32_32x32x16_bf16 v[96:111], v[248:251], v[140:143], v[96:111]
	ds_read_b128 v[128:131], v182 offset:0
	ds_read_b128 v[132:135], v182 offset:0x2000
	ds_read_b128 v[136:139], v181 offset:0
	ds_read_b128 v[236:239], v183 offset:0
	ds_read_b128 v[240:243], v183 offset:0x2000
	ds_read_b128 v[244:247], v181 offset:0x400
	s_waitcnt lgkmcnt(3)
	s_nop 0
	v_mfma_f32_32x32x16_bf16 v[144:159], v[128:131], v[136:139], 0
	v_mfma_f32_32x32x16_bf16 v[128:143], v[132:135], v[136:139], 0
	ds_read_b128 v[248:251], v184 offset:0
	ds_read_b128 v[194:197], v184 offset:0x2000
	ds_read_b128 v[222:225], v181 offset:0x800
	s_waitcnt lgkmcnt(3)
	v_mfma_f32_32x32x16_bf16 v[144:159], v[236:239], v[244:247], v[144:159]
	v_mfma_f32_32x32x16_bf16 v[128:143], v[240:243], v[244:247], v[128:143]
	ds_read_b128 v[236:239], v185 offset:0
	ds_read_b128 v[240:243], v185 offset:0x2000
	ds_read_b128 v[244:247], v181 offset:0xc00
	s_waitcnt lgkmcnt(3)
	v_mfma_f32_32x32x16_bf16 v[144:159], v[248:251], v[222:225], v[144:159]
	v_mfma_f32_32x32x16_bf16 v[128:143], v[194:197], v[222:225], v[128:143]
	ds_read_b128 v[194:197], v182 offset:0x80
	ds_read_b128 v[222:225], v182 offset:0x2080
	ds_read_b128 v[248:251], v181 offset:0x1000
	s_waitcnt lgkmcnt(3)
	v_mfma_f32_32x32x16_bf16 v[144:159], v[236:239], v[244:247], v[144:159]
	v_mfma_f32_32x32x16_bf16 v[128:143], v[240:243], v[244:247], v[128:143]
	ds_read_b128 v[236:239], v183 offset:0x80
	ds_read_b128 v[240:243], v183 offset:0x2080
	ds_read_b128 v[244:247], v181 offset:0x1400
	s_waitcnt lgkmcnt(3)
	v_mfma_f32_32x32x16_bf16 v[144:159], v[194:197], v[248:251], v[144:159]
	v_mfma_f32_32x32x16_bf16 v[128:143], v[222:225], v[248:251], v[128:143]
	ds_read_b128 v[194:197], v184 offset:0x80
	ds_read_b128 v[222:225], v184 offset:0x2080
	ds_read_b128 v[248:251], v181 offset:0x1800
	s_waitcnt lgkmcnt(3)
	v_mfma_f32_32x32x16_bf16 v[144:159], v[236:239], v[244:247], v[144:159]
	v_mfma_f32_32x32x16_bf16 v[128:143], v[240:243], v[244:247], v[128:143]
	ds_read_b128 v[236:239], v185 offset:0x80
	ds_read_b128 v[240:243], v185 offset:0x2080
	s_waitcnt lgkmcnt(2)
	v_mfma_f32_32x32x16_bf16 v[144:159], v[194:197], v[248:251], v[144:159]
	v_mfma_f32_32x32x16_bf16 v[128:143], v[222:225], v[248:251], v[128:143]
	s_waitcnt lgkmcnt(0)
	v_mfma_f32_32x32x16_bf16 v[144:159], v[236:239], v[166:169], v[144:159]
	v_mfma_f32_32x32x16_bf16 v[128:143], v[240:243], v[166:169], v[128:143]
	s_bitcmp0_b32 s100, 8
	s_cbranch_scc1 .Lstg_a3
	s_waitcnt vmcnt(0)
	s_waitcnt lgkmcnt(0)
	s_barrier
	s_sleep 5

.LBB0_539:
	ds_read_b64_tr_b16 v[144:145], v177 offset:0
	ds_read_b64_tr_b16 v[146:147], v177 offset:0x1000
	ds_read_b64_tr_b16 v[148:149], v177 offset:0x2000
	ds_read_b64_tr_b16 v[150:151], v177 offset:0x3000
	ds_read_b64_tr_b16 v[152:153], v177 offset:0x4000
	ds_read_b64_tr_b16 v[154:155], v177 offset:0x5000
	ds_read_b64_tr_b16 v[156:157], v177 offset:0x6000
	ds_read_b64_tr_b16 v[158:159], v177 offset:0x7000
	s_waitcnt lgkmcnt(6)
	s_nop 0
	v_mfma_f32_32x32x16_bf16 v[112:127], v[144:147], v[128:131], v[112:127]
	ds_read_b64_tr_b16 v[170:171], v177 offset:0x200
	ds_read_b64_tr_b16 v[172:173], v177 offset:0x1200
	s_waitcnt lgkmcnt(6)
	v_mfma_f32_32x32x16_bf16 v[112:127], v[148:151], v[132:135], v[112:127]
	ds_read_b64_tr_b16 v[182:183], v177 offset:0x2200
	ds_read_b64_tr_b16 v[184:185], v177 offset:0x3200
	s_waitcnt lgkmcnt(6)
	v_mfma_f32_32x32x16_bf16 v[112:127], v[152:155], v[136:139], v[112:127]
	ds_read_b64_tr_b16 v[190:191], v177 offset:0x4200
	ds_read_b64_tr_b16 v[192:193], v177 offset:0x5200
	s_waitcnt lgkmcnt(6)
	v_mfma_f32_32x32x16_bf16 v[112:127], v[156:159], v[140:143], v[112:127]
	ds_read_b64_tr_b16 v[198:199], v177 offset:0x6200
	ds_read_b64_tr_b16 v[200:201], v177 offset:0x7200
	s_waitcnt lgkmcnt(6)
	v_mfma_f32_32x32x16_bf16 v[0:15], v[170:173], v[128:131], v[0:15]
	ds_read_b64_tr_b16 v[144:145], v177 offset:0x400
	ds_read_b64_tr_b16 v[146:147], v177 offset:0x1400
	s_waitcnt lgkmcnt(6)
	v_mfma_f32_32x32x16_bf16 v[0:15], v[182:185], v[132:135], v[0:15]
	ds_read_b64_tr_b16 v[148:149], v177 offset:0x2400
	ds_read_b64_tr_b16 v[150:151], v177 offset:0x3400
	s_waitcnt lgkmcnt(6)
	v_mfma_f32_32x32x16_bf16 v[0:15], v[190:193], v[136:139], v[0:15]
	ds_read_b64_tr_b16 v[152:153], v177 offset:0x4400
	ds_read_b64_tr_b16 v[154:155], v177 offset:0x5400
	s_waitcnt lgkmcnt(6)
	v_mfma_f32_32x32x16_bf16 v[0:15], v[198:201], v[140:143], v[0:15]
	ds_read_b64_tr_b16 v[156:157], v177 offset:0x6400
	ds_read_b64_tr_b16 v[158:159], v177 offset:0x7400
	s_waitcnt lgkmcnt(6)
	v_mfma_f32_32x32x16_bf16 v[16:31], v[144:147], v[128:131], v[16:31]
	ds_read_b64_tr_b16 v[170:171], v177 offset:0x600
	ds_read_b64_tr_b16 v[172:173], v177 offset:0x1600
	s_waitcnt lgkmcnt(6)
	v_mfma_f32_32x32x16_bf16 v[16:31], v[148:151], v[132:135], v[16:31]
	ds_read_b64_tr_b16 v[182:183], v177 offset:0x2600
	ds_read_b64_tr_b16 v[184:185], v177 offset:0x3600
	s_waitcnt lgkmcnt(6)
	v_mfma_f32_32x32x16_bf16 v[16:31], v[152:155], v[136:139], v[16:31]
	ds_read_b64_tr_b16 v[190:191], v177 offset:0x4600
	ds_read_b64_tr_b16 v[192:193], v177 offset:0x5600
	s_waitcnt lgkmcnt(6)
	v_mfma_f32_32x32x16_bf16 v[16:31], v[156:159], v[140:143], v[16:31]
	ds_read_b64_tr_b16 v[198:199], v177 offset:0x6600
	ds_read_b64_tr_b16 v[200:201], v177 offset:0x7600
	s_waitcnt lgkmcnt(6)
	v_mfma_f32_32x32x16_bf16 v[32:47], v[170:173], v[128:131], v[32:47]
	ds_read_b64_tr_b16 v[144:145], v177 offset:0x800
	ds_read_b64_tr_b16 v[146:147], v177 offset:0x1800
	s_waitcnt lgkmcnt(6)
	v_mfma_f32_32x32x16_bf16 v[32:47], v[182:185], v[132:135], v[32:47]
	ds_read_b64_tr_b16 v[148:149], v177 offset:0x2800
	ds_read_b64_tr_b16 v[150:151], v177 offset:0x3800
	s_waitcnt lgkmcnt(6)
	v_mfma_f32_32x32x16_bf16 v[32:47], v[190:193], v[136:139], v[32:47]
	ds_read_b64_tr_b16 v[152:153], v177 offset:0x4800
	ds_read_b64_tr_b16 v[154:155], v177 offset:0x5800
	s_waitcnt lgkmcnt(6)
	v_mfma_f32_32x32x16_bf16 v[32:47], v[198:201], v[140:143], v[32:47]
	ds_read_b64_tr_b16 v[156:157], v177 offset:0x6800
	ds_read_b64_tr_b16 v[158:159], v177 offset:0x7800
	s_waitcnt lgkmcnt(6)
	v_mfma_f32_32x32x16_bf16 v[48:63], v[144:147], v[128:131], v[48:63]
	ds_read_b64_tr_b16 v[170:171], v177 offset:0xa00
	ds_read_b64_tr_b16 v[172:173], v177 offset:0x1a00
	s_waitcnt lgkmcnt(6)
	v_mfma_f32_32x32x16_bf16 v[48:63], v[148:151], v[132:135], v[48:63]
	ds_read_b64_tr_b16 v[182:183], v177 offset:0x2a00
	ds_read_b64_tr_b16 v[184:185], v177 offset:0x3a00
	s_waitcnt lgkmcnt(6)
	v_mfma_f32_32x32x16_bf16 v[48:63], v[152:155], v[136:139], v[48:63]
	ds_read_b64_tr_b16 v[190:191], v177 offset:0x4a00
	ds_read_b64_tr_b16 v[192:193], v177 offset:0x5a00
	s_waitcnt lgkmcnt(6)
	v_mfma_f32_32x32x16_bf16 v[48:63], v[156:159], v[140:143], v[48:63]
	ds_read_b64_tr_b16 v[198:199], v177 offset:0x6a00
	ds_read_b64_tr_b16 v[200:201], v177 offset:0x7a00
	s_waitcnt lgkmcnt(6)
	v_mfma_f32_32x32x16_bf16 v[64:79], v[170:173], v[128:131], v[64:79]
	ds_read_b64_tr_b16 v[144:145], v177 offset:0xc00
	ds_read_b64_tr_b16 v[146:147], v177 offset:0x1c00
	s_waitcnt lgkmcnt(6)
	v_mfma_f32_32x32x16_bf16 v[64:79], v[182:185], v[132:135], v[64:79]
	ds_read_b64_tr_b16 v[148:149], v177 offset:0x2c00
	ds_read_b64_tr_b16 v[150:151], v177 offset:0x3c00
	s_waitcnt lgkmcnt(6)
	v_mfma_f32_32x32x16_bf16 v[64:79], v[190:193], v[136:139], v[64:79]
	ds_read_b64_tr_b16 v[152:153], v177 offset:0x4c00
	ds_read_b64_tr_b16 v[154:155], v177 offset:0x5c00
	s_waitcnt lgkmcnt(6)
	v_mfma_f32_32x32x16_bf16 v[64:79], v[198:201], v[140:143], v[64:79]
	ds_read_b64_tr_b16 v[156:157], v177 offset:0x6c00
	ds_read_b64_tr_b16 v[158:159], v177 offset:0x7c00
	s_waitcnt lgkmcnt(6)
	v_mfma_f32_32x32x16_bf16 v[80:95], v[144:147], v[128:131], v[80:95]
	ds_read_b64_tr_b16 v[170:171], v177 offset:0xe00
	ds_read_b64_tr_b16 v[172:173], v177 offset:0x1e00
	s_waitcnt lgkmcnt(6)
	v_mfma_f32_32x32x16_bf16 v[80:95], v[148:151], v[132:135], v[80:95]
	ds_read_b64_tr_b16 v[182:183], v177 offset:0x2e00
	ds_read_b64_tr_b16 v[184:185], v177 offset:0x3e00
	s_waitcnt lgkmcnt(6)
	v_mfma_f32_32x32x16_bf16 v[80:95], v[152:155], v[136:139], v[80:95]
	ds_read_b64_tr_b16 v[190:191], v177 offset:0x4e00
	ds_read_b64_tr_b16 v[192:193], v177 offset:0x5e00
	s_waitcnt lgkmcnt(6)
	v_mfma_f32_32x32x16_bf16 v[80:95], v[156:159], v[140:143], v[80:95]
	ds_read_b64_tr_b16 v[198:199], v177 offset:0x6e00
	ds_read_b64_tr_b16 v[200:201], v177 offset:0x7e00
	s_waitcnt lgkmcnt(6)
	v_mfma_f32_32x32x16_bf16 v[96:111], v[170:173], v[128:131], v[96:111]
	s_waitcnt lgkmcnt(4)
	v_mfma_f32_32x32x16_bf16 v[96:111], v[182:185], v[132:135], v[96:111]
	s_waitcnt lgkmcnt(2)
	v_mfma_f32_32x32x16_bf16 v[96:111], v[190:193], v[136:139], v[96:111]
	s_waitcnt lgkmcnt(0)
	v_mfma_f32_32x32x16_bf16 v[96:111], v[198:201], v[140:143], v[96:111]
	ds_read_b128 v[128:131], v189 offset:0
	ds_read_b128 v[132:135], v189 offset:0x2000
	ds_read_b128 v[136:139], v181 offset:0
	ds_read_b128 v[170:173], v188 offset:0
	ds_read_b128 v[182:185], v188 offset:0x2000
	ds_read_b128 v[190:193], v181 offset:0x400
	s_waitcnt lgkmcnt(3)
	s_nop 0
	v_mfma_f32_32x32x16_bf16 v[144:159], v[128:131], v[136:139], 0
	v_mfma_f32_32x32x16_bf16 v[128:143], v[132:135], v[136:139], 0
	ds_read_b128 v[198:201], v187 offset:0
	ds_read_b128 v[202:205], v187 offset:0x2000
	ds_read_b128 v[206:209], v181 offset:0x800
	s_waitcnt lgkmcnt(3)
	v_mfma_f32_32x32x16_bf16 v[144:159], v[170:173], v[190:193], v[144:159]
	v_mfma_f32_32x32x16_bf16 v[128:143], v[182:185], v[190:193], v[128:143]
	ds_read_b128 v[170:173], v186 offset:0
	ds_read_b128 v[182:185], v186 offset:0x2000
	ds_read_b128 v[190:193], v181 offset:0xc00
	s_waitcnt lgkmcnt(3)
	v_mfma_f32_32x32x16_bf16 v[144:159], v[198:201], v[206:209], v[144:159]
	v_mfma_f32_32x32x16_bf16 v[128:143], v[202:205], v[206:209], v[128:143]
	ds_read_b128 v[198:201], v189 offset:0x80
	ds_read_b128 v[202:205], v189 offset:0x2080
	ds_read_b128 v[206:209], v181 offset:0x1000
	s_waitcnt lgkmcnt(3)
	v_mfma_f32_32x32x16_bf16 v[144:159], v[170:173], v[190:193], v[144:159]
	v_mfma_f32_32x32x16_bf16 v[128:143], v[182:185], v[190:193], v[128:143]
	ds_read_b128 v[170:173], v188 offset:0x80
	ds_read_b128 v[182:185], v188 offset:0x2080
	ds_read_b128 v[188:191], v181 offset:0x1400
	s_waitcnt lgkmcnt(3)
	v_mfma_f32_32x32x16_bf16 v[144:159], v[198:201], v[206:209], v[144:159]
	v_mfma_f32_32x32x16_bf16 v[128:143], v[202:205], v[206:209], v[128:143]
	ds_read_b128 v[198:201], v187 offset:0x80
	ds_read_b128 v[202:205], v187 offset:0x2080
	ds_read_b128 v[206:209], v181 offset:0x1800
	s_waitcnt lgkmcnt(3)
	v_mfma_f32_32x32x16_bf16 v[144:159], v[170:173], v[188:191], v[144:159]
	v_mfma_f32_32x32x16_bf16 v[128:143], v[182:185], v[188:191], v[128:143]
	ds_read_b128 v[170:173], v186 offset:0x80
	ds_read_b128 v[182:185], v186 offset:0x2080
	s_waitcnt lgkmcnt(2)
	v_mfma_f32_32x32x16_bf16 v[144:159], v[198:201], v[206:209], v[144:159]
	v_mfma_f32_32x32x16_bf16 v[128:143], v[202:205], v[206:209], v[128:143]
	s_waitcnt lgkmcnt(0)
	v_mfma_f32_32x32x16_bf16 v[144:159], v[170:173], v[166:169], v[144:159]
	v_mfma_f32_32x32x16_bf16 v[128:143], v[182:185], v[166:169], v[128:143]
	s_bitcmp0_b32 s100, 8
	s_cbranch_scc1 .Lstg_a4
	s_waitcnt vmcnt(0)
	s_waitcnt lgkmcnt(0)
	s_barrier
	s_sleep 5

.LBB0_554:
	s_or_b64 exec, exec, s[4:5]
	s_ashr_i32 s95, s94, 31
	s_add_u32 s4, s2, s16
	s_addc_u32 s3, s3, 0
	v_mov_b32_e32 v38, v165
	s_add_u32 s2, s4, 0x2800
	s_addc_u32 s33, s3, 0
	v_readfirstlane_b32 s5, v38
	s_ashr_i32 s79, s5, 6
	v_bfe_u32 v0, v38, 5, 1
	v_and_b32_e32 v175, 31, v38
	s_lshl_b32 s92, s79, 5
	v_lshlrev_b32_e32 v32, 2, v0
	s_add_i32 s82, s92, s78
	v_sub_u32_e32 v1, v175, v32
	v_lshlrev_b32_e32 v176, 4, v0
	s_lshl_b32 s76, s79, 3
	v_bfe_u32 v0, v38, 4, 2
	v_writelane_b32 v255, s16, 17
	v_add_u32_e32 v179, s82, v1
	v_or_b32_e32 v1, s76, v0
	v_and_b32_e32 v2, 15, v38
	s_lshl_b32 s5, s79, 12
	v_and_b32_e32 v39, 63, v38
	v_bitop3_b32 v3, v0, v38, 15 bitop3:0x78
	v_mul_lo_u32 v1, v1, s84
	v_bitop3_b32 v0, v0, v2, 4 bitop3:0x36
	s_add_i32 s93, s5, s77
	s_mul_i32 s5, s79, 0x1c00
	v_readlane_b32 s7, v255, 51
	s_waitcnt vmcnt(16)
	v_lshlrev_b32_e32 v40, 4, v39
	v_lshl_or_b32 v0, v0, 4, v1
	s_lshl_b32 s83, s79, 11
	v_readlane_b32 s6, v255, 53
	s_add_i32 s5, s7, s5
	v_lshl_or_b32 v160, v3, 4, v1
	v_add_u32_e32 v170, 0x1a000, v0
	s_add_i32 s83, s83, s6
	v_add_u32_e32 v180, s5, v40
	s_waitcnt vmcnt(16) lgkmcnt(0)
	ds_write_b128 v180, v[128:131]
	ds_write_b128 v180, v[132:135] offset:1024
	ds_write_b128 v180, v[136:139] offset:2048
	ds_write_b128 v180, v[140:143] offset:3072
	ds_write_b128 v180, v[144:147] offset:4096
	ds_write_b128 v180, v[148:151] offset:5120
	ds_write_b128 v180, v[152:155] offset:6144
	s_add_u32 s4, s4, 0x1a2800
	s_addc_u32 s5, s3, 0
	v_lshl_add_u64 v[0:1], s[4:5], 0, v[160:161]
	s_add_i32 s84, s83, 0x4000
	s_mov_b32 s3, m0
	s_mov_b32 m0, s84
	s_nop 0
	global_load_lds_dwordx4 v[0:1], off
	s_mov_b32 m0, s3
	v_mov_b32_e32 v171, v161
	v_lshl_add_u64 v[0:1], s[4:5], 0, v[170:171]
	s_add_i32 s85, s83, 0x4400
	s_mov_b32 s3, m0
	s_mov_b32 m0, s85
	s_nop 0
	global_load_lds_dwordx4 v[0:1], off
	s_mov_b32 m0, s3
	s_waitcnt lgkmcnt(0)
	s_barrier
	v_lshlrev_b32_e32 v0, 4, v38
	s_movk_i32 s3, 0x70
	v_lshlrev_b32_e32 v33, 8, v175
	v_and_b32_e32 v1, 0x70, v0
	v_bitop3_b32 v34, v176, v0, s3 bitop3:0x78
	s_movk_i32 s3, 0x60
	v_add_u32_e32 v2, s6, v33
	v_bitop3_b32 v35, v176, v1, 32 bitop3:0x36
	v_bitop3_b32 v36, v176, v1, 64 bitop3:0x36
	v_bitop3_b32 v37, v176, v1, s3 bitop3:0x36
	v_add_u32_e32 v181, v34, v2
	v_add_u32_e32 v182, v35, v2
	v_add_u32_e32 v183, v36, v2
	v_add_u32_e32 v184, v37, v2
	ds_read_b128 v[0:3], v181 offset:0
	ds_read_b128 v[4:7], v181 offset:0x2000
	ds_read_b128 v[8:11], v180 offset:0
	ds_read_b128 v[42:45], v182 offset:0
	ds_read_b128 v[46:49], v182 offset:0x2000
	ds_read_b128 v[50:53], v180 offset:0x400
	s_waitcnt lgkmcnt(3)
	s_nop 0
	v_mfma_f32_32x32x16_bf16 v[16:31], v[0:3], v[8:11], 0
	v_mfma_f32_32x32x16_bf16 v[0:15], v[4:7], v[8:11], 0
	ds_read_b128 v[54:57], v183 offset:0
	ds_read_b128 v[58:61], v183 offset:0x2000
	ds_read_b128 v[62:65], v180 offset:0x800
	s_waitcnt lgkmcnt(3)
	v_mfma_f32_32x32x16_bf16 v[16:31], v[42:45], v[50:53], v[16:31]
	v_mfma_f32_32x32x16_bf16 v[0:15], v[46:49], v[50:53], v[0:15]
	ds_read_b128 v[42:45], v184 offset:0
	ds_read_b128 v[46:49], v184 offset:0x2000
	ds_read_b128 v[50:53], v180 offset:0xc00
	s_waitcnt lgkmcnt(3)
	v_mfma_f32_32x32x16_bf16 v[16:31], v[54:57], v[62:65], v[16:31]
	v_mfma_f32_32x32x16_bf16 v[0:15], v[58:61], v[62:65], v[0:15]
	ds_read_b128 v[54:57], v181 offset:0x80
	ds_read_b128 v[58:61], v181 offset:0x2080
	ds_read_b128 v[62:65], v180 offset:0x1000
	s_waitcnt lgkmcnt(3)
	v_mfma_f32_32x32x16_bf16 v[16:31], v[42:45], v[50:53], v[16:31]
	v_mfma_f32_32x32x16_bf16 v[0:15], v[46:49], v[50:53], v[0:15]
	ds_read_b128 v[42:45], v182 offset:0x80
	ds_read_b128 v[46:49], v182 offset:0x2080
	ds_read_b128 v[50:53], v180 offset:0x1400
	s_waitcnt lgkmcnt(3)
	v_mfma_f32_32x32x16_bf16 v[16:31], v[54:57], v[62:65], v[16:31]
	v_mfma_f32_32x32x16_bf16 v[0:15], v[58:61], v[62:65], v[0:15]
	ds_read_b128 v[54:57], v183 offset:0x80
	ds_read_b128 v[58:61], v183 offset:0x2080
	ds_read_b128 v[62:65], v180 offset:0x1800
	s_waitcnt lgkmcnt(3)
	v_mfma_f32_32x32x16_bf16 v[16:31], v[42:45], v[50:53], v[16:31]
	v_mfma_f32_32x32x16_bf16 v[0:15], v[46:49], v[50:53], v[0:15]
	ds_read_b128 v[42:45], v184 offset:0x80
	ds_read_b128 v[46:49], v184 offset:0x2080
	s_waitcnt lgkmcnt(2)
	v_mfma_f32_32x32x16_bf16 v[16:31], v[54:57], v[62:65], v[16:31]
	v_mfma_f32_32x32x16_bf16 v[0:15], v[58:61], v[62:65], v[0:15]
	s_waitcnt lgkmcnt(0)
	v_mfma_f32_32x32x16_bf16 v[16:31], v[42:45], v[166:169], v[16:31]
	v_mfma_f32_32x32x16_bf16 v[0:15], v[46:49], v[166:169], v[0:15]
	s_bitcmp0_b32 s100, 8
	s_cbranch_scc1 .Lstg_a9
	s_waitcnt vmcnt(0)
	s_waitcnt lgkmcnt(0)
	s_barrier
	s_sleep 5

.LBB0_557:
	ds_read_b64_tr_b16 v[144:145], v177 offset:0
	ds_read_b64_tr_b16 v[146:147], v177 offset:0x1000
	ds_read_b64_tr_b16 v[148:149], v177 offset:0x2000
	ds_read_b64_tr_b16 v[150:151], v177 offset:0x3000
	ds_read_b64_tr_b16 v[152:153], v177 offset:0x4000
	ds_read_b64_tr_b16 v[154:155], v177 offset:0x5000
	ds_read_b64_tr_b16 v[156:157], v177 offset:0x6000
	ds_read_b64_tr_b16 v[158:159], v177 offset:0x7000
	s_waitcnt lgkmcnt(6)
	s_nop 0
	v_mfma_f32_32x32x16_bf16 v[112:127], v[144:147], v[128:131], v[112:127]
	ds_read_b64_tr_b16 v[192:193], v177 offset:0x200
	ds_read_b64_tr_b16 v[194:195], v177 offset:0x1200
	s_waitcnt lgkmcnt(6)
	v_mfma_f32_32x32x16_bf16 v[112:127], v[148:151], v[132:135], v[112:127]
	ds_read_b64_tr_b16 v[196:197], v177 offset:0x2200
	ds_read_b64_tr_b16 v[198:199], v177 offset:0x3200
	s_waitcnt lgkmcnt(6)
	v_mfma_f32_32x32x16_bf16 v[112:127], v[152:155], v[136:139], v[112:127]
	ds_read_b64_tr_b16 v[200:201], v177 offset:0x4200
	ds_read_b64_tr_b16 v[202:203], v177 offset:0x5200
	s_waitcnt lgkmcnt(6)
	v_mfma_f32_32x32x16_bf16 v[112:127], v[156:159], v[140:143], v[112:127]
	ds_read_b64_tr_b16 v[204:205], v177 offset:0x6200
	ds_read_b64_tr_b16 v[206:207], v177 offset:0x7200
	s_waitcnt lgkmcnt(6)
	v_mfma_f32_32x32x16_bf16 v[80:95], v[192:195], v[128:131], v[80:95]
	ds_read_b64_tr_b16 v[144:145], v177 offset:0x400
	ds_read_b64_tr_b16 v[146:147], v177 offset:0x1400
	s_waitcnt lgkmcnt(6)
	v_mfma_f32_32x32x16_bf16 v[80:95], v[196:199], v[132:135], v[80:95]
	ds_read_b64_tr_b16 v[148:149], v177 offset:0x2400
	ds_read_b64_tr_b16 v[150:151], v177 offset:0x3400
	s_waitcnt lgkmcnt(6)
	v_mfma_f32_32x32x16_bf16 v[80:95], v[200:203], v[136:139], v[80:95]
	ds_read_b64_tr_b16 v[152:153], v177 offset:0x4400
	ds_read_b64_tr_b16 v[154:155], v177 offset:0x5400
	s_waitcnt lgkmcnt(6)
	v_mfma_f32_32x32x16_bf16 v[80:95], v[204:207], v[140:143], v[80:95]
	ds_read_b64_tr_b16 v[156:157], v177 offset:0x6400
	ds_read_b64_tr_b16 v[158:159], v177 offset:0x7400
	s_waitcnt lgkmcnt(6)
	v_mfma_f32_32x32x16_bf16 v[96:111], v[144:147], v[128:131], v[96:111]
	ds_read_b64_tr_b16 v[192:193], v177 offset:0x600
	ds_read_b64_tr_b16 v[194:195], v177 offset:0x1600
	s_waitcnt lgkmcnt(6)
	v_mfma_f32_32x32x16_bf16 v[96:111], v[148:151], v[132:135], v[96:111]
	ds_read_b64_tr_b16 v[196:197], v177 offset:0x2600
	ds_read_b64_tr_b16 v[198:199], v177 offset:0x3600
	s_waitcnt lgkmcnt(6)
	v_mfma_f32_32x32x16_bf16 v[96:111], v[152:155], v[136:139], v[96:111]
	ds_read_b64_tr_b16 v[200:201], v177 offset:0x4600
	ds_read_b64_tr_b16 v[202:203], v177 offset:0x5600
	s_waitcnt lgkmcnt(6)
	v_mfma_f32_32x32x16_bf16 v[96:111], v[156:159], v[140:143], v[96:111]
	ds_read_b64_tr_b16 v[204:205], v177 offset:0x6600
	ds_read_b64_tr_b16 v[206:207], v177 offset:0x7600
	s_waitcnt lgkmcnt(6)
	v_mfma_f32_32x32x16_bf16 v[64:79], v[192:195], v[128:131], v[64:79]
	ds_read_b64_tr_b16 v[144:145], v177 offset:0x800
	ds_read_b64_tr_b16 v[146:147], v177 offset:0x1800
	s_waitcnt lgkmcnt(6)
	v_mfma_f32_32x32x16_bf16 v[64:79], v[196:199], v[132:135], v[64:79]
	ds_read_b64_tr_b16 v[148:149], v177 offset:0x2800
	ds_read_b64_tr_b16 v[150:151], v177 offset:0x3800
	s_waitcnt lgkmcnt(6)
	v_mfma_f32_32x32x16_bf16 v[64:79], v[200:203], v[136:139], v[64:79]
	ds_read_b64_tr_b16 v[152:153], v177 offset:0x4800
	ds_read_b64_tr_b16 v[154:155], v177 offset:0x5800
	s_waitcnt lgkmcnt(6)
	v_mfma_f32_32x32x16_bf16 v[64:79], v[204:207], v[140:143], v[64:79]
	ds_read_b64_tr_b16 v[156:157], v177 offset:0x6800
	ds_read_b64_tr_b16 v[158:159], v177 offset:0x7800
	s_waitcnt lgkmcnt(6)
	v_mfma_f32_32x32x16_bf16 v[48:63], v[144:147], v[128:131], v[48:63]
	ds_read_b64_tr_b16 v[192:193], v177 offset:0xa00
	ds_read_b64_tr_b16 v[194:195], v177 offset:0x1a00
	s_waitcnt lgkmcnt(6)
	v_mfma_f32_32x32x16_bf16 v[48:63], v[148:151], v[132:135], v[48:63]
	ds_read_b64_tr_b16 v[196:197], v177 offset:0x2a00
	ds_read_b64_tr_b16 v[198:199], v177 offset:0x3a00
	s_waitcnt lgkmcnt(6)
	v_mfma_f32_32x32x16_bf16 v[48:63], v[152:155], v[136:139], v[48:63]
	ds_read_b64_tr_b16 v[200:201], v177 offset:0x4a00
	ds_read_b64_tr_b16 v[202:203], v177 offset:0x5a00
	s_waitcnt lgkmcnt(6)
	v_mfma_f32_32x32x16_bf16 v[48:63], v[156:159], v[140:143], v[48:63]
	ds_read_b64_tr_b16 v[204:205], v177 offset:0x6a00
	ds_read_b64_tr_b16 v[206:207], v177 offset:0x7a00
	s_waitcnt lgkmcnt(6)
	v_mfma_f32_32x32x16_bf16 v[32:47], v[192:195], v[128:131], v[32:47]
	ds_read_b64_tr_b16 v[144:145], v177 offset:0xc00
	ds_read_b64_tr_b16 v[146:147], v177 offset:0x1c00
	s_waitcnt lgkmcnt(6)
	v_mfma_f32_32x32x16_bf16 v[32:47], v[196:199], v[132:135], v[32:47]
	ds_read_b64_tr_b16 v[148:149], v177 offset:0x2c00
	ds_read_b64_tr_b16 v[150:151], v177 offset:0x3c00
	s_waitcnt lgkmcnt(6)
	v_mfma_f32_32x32x16_bf16 v[32:47], v[200:203], v[136:139], v[32:47]
	ds_read_b64_tr_b16 v[152:153], v177 offset:0x4c00
	ds_read_b64_tr_b16 v[154:155], v177 offset:0x5c00
	s_waitcnt lgkmcnt(6)
	v_mfma_f32_32x32x16_bf16 v[32:47], v[204:207], v[140:143], v[32:47]
	ds_read_b64_tr_b16 v[156:157], v177 offset:0x6c00
	ds_read_b64_tr_b16 v[158:159], v177 offset:0x7c00
	s_waitcnt lgkmcnt(6)
	v_mfma_f32_32x32x16_bf16 v[16:31], v[144:147], v[128:131], v[16:31]
	ds_read_b64_tr_b16 v[192:193], v177 offset:0xe00
	ds_read_b64_tr_b16 v[194:195], v177 offset:0x1e00
	s_waitcnt lgkmcnt(6)
	v_mfma_f32_32x32x16_bf16 v[16:31], v[148:151], v[132:135], v[16:31]
	ds_read_b64_tr_b16 v[196:197], v177 offset:0x2e00
	ds_read_b64_tr_b16 v[198:199], v177 offset:0x3e00
	s_waitcnt lgkmcnt(6)
	v_mfma_f32_32x32x16_bf16 v[16:31], v[152:155], v[136:139], v[16:31]
	ds_read_b64_tr_b16 v[200:201], v177 offset:0x4e00
	ds_read_b64_tr_b16 v[202:203], v177 offset:0x5e00
	s_waitcnt lgkmcnt(6)
	v_mfma_f32_32x32x16_bf16 v[16:31], v[156:159], v[140:143], v[16:31]
	ds_read_b64_tr_b16 v[204:205], v177 offset:0x6e00
	ds_read_b64_tr_b16 v[206:207], v177 offset:0x7e00
	s_waitcnt lgkmcnt(6)
	v_mfma_f32_32x32x16_bf16 v[0:15], v[192:195], v[128:131], v[0:15]
	ds_read_b128 v[236:239], v188 offset:0
	ds_read_b128 v[240:243], v188 offset:0x2000
	s_waitcnt lgkmcnt(6)
	v_mfma_f32_32x32x16_bf16 v[0:15], v[196:199], v[132:135], v[0:15]
	ds_read_b128 v[244:247], v180 offset:0
	ds_read_b128 v[248:251], v187 offset:0
	s_waitcnt lgkmcnt(6)
	v_mfma_f32_32x32x16_bf16 v[0:15], v[200:203], v[136:139], v[0:15]
	ds_read_b128 v[218:221], v187 offset:0x2000
	ds_read_b128 v[222:225], v180 offset:0x400
	s_waitcnt lgkmcnt(6)
	v_mfma_f32_32x32x16_bf16 v[0:15], v[204:207], v[140:143], v[0:15]
	s_waitcnt lgkmcnt(3)
	s_nop 0
	v_mfma_f32_32x32x16_bf16 v[144:159], v[236:239], v[244:247], 0
	ds_read_b128 v[192:195], v186 offset:0
	ds_read_b128 v[196:199], v186 offset:0x2000
	v_mfma_f32_32x32x16_bf16 v[128:143], v[240:243], v[244:247], 0
	ds_read_b128 v[200:203], v180 offset:0x800
	s_waitcnt lgkmcnt(3)
	v_mfma_f32_32x32x16_bf16 v[144:159], v[248:251], v[222:225], v[144:159]
	ds_read_b128 v[236:239], v185 offset:0
	ds_read_b128 v[240:243], v185 offset:0x2000
	v_mfma_f32_32x32x16_bf16 v[128:143], v[218:221], v[222:225], v[128:143]
	ds_read_b128 v[244:247], v180 offset:0xc00
	s_waitcnt lgkmcnt(3)
	v_mfma_f32_32x32x16_bf16 v[144:159], v[192:195], v[200:203], v[144:159]
	ds_read_b128 v[248:251], v188 offset:0x80
	ds_read_b128 v[218:221], v188 offset:0x2080
	v_mfma_f32_32x32x16_bf16 v[128:143], v[196:199], v[200:203], v[128:143]
	ds_read_b128 v[222:225], v180 offset:0x1000
	s_waitcnt lgkmcnt(3)
	v_mfma_f32_32x32x16_bf16 v[144:159], v[236:239], v[244:247], v[144:159]
	ds_read_b128 v[192:195], v187 offset:0x80
	ds_read_b128 v[196:199], v187 offset:0x2080
	v_mfma_f32_32x32x16_bf16 v[128:143], v[240:243], v[244:247], v[128:143]
	ds_read_b128 v[200:203], v180 offset:0x1400
	s_waitcnt lgkmcnt(3)
	v_mfma_f32_32x32x16_bf16 v[144:159], v[248:251], v[222:225], v[144:159]
	ds_read_b128 v[236:239], v186 offset:0x80
	ds_read_b128 v[240:243], v186 offset:0x2080
	v_mfma_f32_32x32x16_bf16 v[128:143], v[218:221], v[222:225], v[128:143]
	ds_read_b128 v[244:247], v180 offset:0x1800
	s_waitcnt lgkmcnt(3)
	v_mfma_f32_32x32x16_bf16 v[144:159], v[192:195], v[200:203], v[144:159]
	ds_read_b128 v[248:251], v185 offset:0x80
	ds_read_b128 v[218:221], v185 offset:0x2080
	v_mfma_f32_32x32x16_bf16 v[128:143], v[196:199], v[200:203], v[128:143]
	s_waitcnt lgkmcnt(2)
	v_mfma_f32_32x32x16_bf16 v[144:159], v[236:239], v[244:247], v[144:159]
	v_mfma_f32_32x32x16_bf16 v[128:143], v[240:243], v[244:247], v[128:143]
	s_waitcnt lgkmcnt(0)
	v_mfma_f32_32x32x16_bf16 v[144:159], v[248:251], v[166:169], v[144:159]
	v_mfma_f32_32x32x16_bf16 v[128:143], v[218:221], v[166:169], v[128:143]
	s_bitcmp0_b32 s100, 8
	s_cbranch_scc1 .Lstg_a10
	s_waitcnt vmcnt(0)
	s_waitcnt lgkmcnt(0)
	s_barrier
	s_sleep 5

.LBB0_565:
	ds_read_b64_tr_b16 v[144:145], v177 offset:0x8000
	ds_read_b64_tr_b16 v[146:147], v177 offset:0x9000
	ds_read_b64_tr_b16 v[148:149], v177 offset:0xa000
	ds_read_b64_tr_b16 v[150:151], v177 offset:0xb000
	ds_read_b64_tr_b16 v[152:153], v177 offset:0xc000
	ds_read_b64_tr_b16 v[154:155], v177 offset:0xd000
	ds_read_b64_tr_b16 v[156:157], v177 offset:0xe000
	ds_read_b64_tr_b16 v[158:159], v177 offset:0xf000
	s_waitcnt lgkmcnt(6)
	s_nop 0
	v_mfma_f32_32x32x16_bf16 v[112:127], v[144:147], v[128:131], v[112:127]
	ds_read_b64_tr_b16 v[194:195], v177 offset:0x8200
	ds_read_b64_tr_b16 v[196:197], v177 offset:0x9200
	s_waitcnt lgkmcnt(6)
	v_mfma_f32_32x32x16_bf16 v[112:127], v[148:151], v[132:135], v[112:127]
	ds_read_b64_tr_b16 v[198:199], v177 offset:0xa200
	ds_read_b64_tr_b16 v[200:201], v177 offset:0xb200
	s_waitcnt lgkmcnt(6)
	v_mfma_f32_32x32x16_bf16 v[112:127], v[152:155], v[136:139], v[112:127]
	ds_read_b64_tr_b16 v[202:203], v177 offset:0xc200
	ds_read_b64_tr_b16 v[204:205], v177 offset:0xd200
	s_waitcnt lgkmcnt(6)
	v_mfma_f32_32x32x16_bf16 v[112:127], v[156:159], v[140:143], v[112:127]
	ds_read_b64_tr_b16 v[206:207], v177 offset:0xe200
	ds_read_b64_tr_b16 v[208:209], v177 offset:0xf200
	s_waitcnt lgkmcnt(6)
	v_mfma_f32_32x32x16_bf16 v[80:95], v[194:197], v[128:131], v[80:95]
	ds_read_b64_tr_b16 v[144:145], v177 offset:0x8400
	ds_read_b64_tr_b16 v[146:147], v177 offset:0x9400
	s_waitcnt lgkmcnt(6)
	v_mfma_f32_32x32x16_bf16 v[80:95], v[198:201], v[132:135], v[80:95]
	ds_read_b64_tr_b16 v[148:149], v177 offset:0xa400
	ds_read_b64_tr_b16 v[150:151], v177 offset:0xb400
	s_waitcnt lgkmcnt(6)
	v_mfma_f32_32x32x16_bf16 v[80:95], v[202:205], v[136:139], v[80:95]
	ds_read_b64_tr_b16 v[152:153], v177 offset:0xc400
	ds_read_b64_tr_b16 v[154:155], v177 offset:0xd400
	s_waitcnt lgkmcnt(6)
	v_mfma_f32_32x32x16_bf16 v[80:95], v[206:209], v[140:143], v[80:95]
	ds_read_b64_tr_b16 v[156:157], v177 offset:0xe400
	ds_read_b64_tr_b16 v[158:159], v177 offset:0xf400
	s_waitcnt lgkmcnt(6)
	v_mfma_f32_32x32x16_bf16 v[96:111], v[144:147], v[128:131], v[96:111]
	ds_read_b64_tr_b16 v[194:195], v177 offset:0x8600
	ds_read_b64_tr_b16 v[196:197], v177 offset:0x9600
	s_waitcnt lgkmcnt(6)
	v_mfma_f32_32x32x16_bf16 v[96:111], v[148:151], v[132:135], v[96:111]
	ds_read_b64_tr_b16 v[198:199], v177 offset:0xa600
	ds_read_b64_tr_b16 v[200:201], v177 offset:0xb600
	s_waitcnt lgkmcnt(6)
	v_mfma_f32_32x32x16_bf16 v[96:111], v[152:155], v[136:139], v[96:111]
	ds_read_b64_tr_b16 v[202:203], v177 offset:0xc600
	ds_read_b64_tr_b16 v[204:205], v177 offset:0xd600
	s_waitcnt lgkmcnt(6)
	v_mfma_f32_32x32x16_bf16 v[96:111], v[156:159], v[140:143], v[96:111]
	ds_read_b64_tr_b16 v[206:207], v177 offset:0xe600
	ds_read_b64_tr_b16 v[208:209], v177 offset:0xf600
	s_waitcnt lgkmcnt(6)
	v_mfma_f32_32x32x16_bf16 v[64:79], v[194:197], v[128:131], v[64:79]
	ds_read_b64_tr_b16 v[144:145], v177 offset:0x8800
	ds_read_b64_tr_b16 v[146:147], v177 offset:0x9800
	s_waitcnt lgkmcnt(6)
	v_mfma_f32_32x32x16_bf16 v[64:79], v[198:201], v[132:135], v[64:79]
	ds_read_b64_tr_b16 v[148:149], v177 offset:0xa800
	ds_read_b64_tr_b16 v[150:151], v177 offset:0xb800
	s_waitcnt lgkmcnt(6)
	v_mfma_f32_32x32x16_bf16 v[64:79], v[202:205], v[136:139], v[64:79]
	ds_read_b64_tr_b16 v[152:153], v177 offset:0xc800
	ds_read_b64_tr_b16 v[154:155], v177 offset:0xd800
	s_waitcnt lgkmcnt(6)
	v_mfma_f32_32x32x16_bf16 v[64:79], v[206:209], v[140:143], v[64:79]
	ds_read_b64_tr_b16 v[156:157], v177 offset:0xe800
	ds_read_b64_tr_b16 v[158:159], v177 offset:0xf800
	s_waitcnt lgkmcnt(6)
	v_mfma_f32_32x32x16_bf16 v[48:63], v[144:147], v[128:131], v[48:63]
	ds_read_b64_tr_b16 v[194:195], v177 offset:0x8a00
	ds_read_b64_tr_b16 v[196:197], v177 offset:0x9a00
	s_waitcnt lgkmcnt(6)
	v_mfma_f32_32x32x16_bf16 v[48:63], v[148:151], v[132:135], v[48:63]
	ds_read_b64_tr_b16 v[198:199], v177 offset:0xaa00
	ds_read_b64_tr_b16 v[200:201], v177 offset:0xba00
	s_waitcnt lgkmcnt(6)
	v_mfma_f32_32x32x16_bf16 v[48:63], v[152:155], v[136:139], v[48:63]
	ds_read_b64_tr_b16 v[202:203], v177 offset:0xca00
	ds_read_b64_tr_b16 v[204:205], v177 offset:0xda00
	s_waitcnt lgkmcnt(6)
	v_mfma_f32_32x32x16_bf16 v[48:63], v[156:159], v[140:143], v[48:63]
	ds_read_b64_tr_b16 v[206:207], v177 offset:0xea00
	ds_read_b64_tr_b16 v[208:209], v177 offset:0xfa00
	s_waitcnt lgkmcnt(6)
	v_mfma_f32_32x32x16_bf16 v[32:47], v[194:197], v[128:131], v[32:47]
	ds_read_b64_tr_b16 v[144:145], v177 offset:0x8c00
	ds_read_b64_tr_b16 v[146:147], v177 offset:0x9c00
	s_waitcnt lgkmcnt(6)
	v_mfma_f32_32x32x16_bf16 v[32:47], v[198:201], v[132:135], v[32:47]
	ds_read_b64_tr_b16 v[148:149], v177 offset:0xac00
	ds_read_b64_tr_b16 v[150:151], v177 offset:0xbc00
	s_waitcnt lgkmcnt(6)
	v_mfma_f32_32x32x16_bf16 v[32:47], v[202:205], v[136:139], v[32:47]
	ds_read_b64_tr_b16 v[152:153], v177 offset:0xcc00
	ds_read_b64_tr_b16 v[154:155], v177 offset:0xdc00
	s_waitcnt lgkmcnt(6)
	v_mfma_f32_32x32x16_bf16 v[32:47], v[206:209], v[140:143], v[32:47]
	ds_read_b64_tr_b16 v[156:157], v177 offset:0xec00
	ds_read_b64_tr_b16 v[158:159], v177 offset:0xfc00
	s_waitcnt lgkmcnt(6)
	v_mfma_f32_32x32x16_bf16 v[16:31], v[144:147], v[128:131], v[16:31]
	ds_read_b64_tr_b16 v[194:195], v177 offset:0x8e00
	ds_read_b64_tr_b16 v[196:197], v177 offset:0x9e00
	s_waitcnt lgkmcnt(6)
	v_mfma_f32_32x32x16_bf16 v[16:31], v[148:151], v[132:135], v[16:31]
	ds_read_b64_tr_b16 v[198:199], v177 offset:0xae00
	ds_read_b64_tr_b16 v[200:201], v177 offset:0xbe00
	s_waitcnt lgkmcnt(6)
	v_mfma_f32_32x32x16_bf16 v[16:31], v[152:155], v[136:139], v[16:31]
	ds_read_b64_tr_b16 v[202:203], v177 offset:0xce00
	ds_read_b64_tr_b16 v[204:205], v177 offset:0xde00
	s_waitcnt lgkmcnt(6)
	v_mfma_f32_32x32x16_bf16 v[16:31], v[156:159], v[140:143], v[16:31]
	ds_read_b64_tr_b16 v[206:207], v177 offset:0xee00
	ds_read_b64_tr_b16 v[208:209], v177 offset:0xfe00
	s_waitcnt lgkmcnt(6)
	v_mfma_f32_32x32x16_bf16 v[0:15], v[194:197], v[128:131], v[0:15]
	ds_read_b128 v[236:239], v181 offset:0
	ds_read_b128 v[240:243], v181 offset:0x2000
	s_waitcnt lgkmcnt(6)
	v_mfma_f32_32x32x16_bf16 v[0:15], v[198:201], v[132:135], v[0:15]
	ds_read_b128 v[244:247], v180 offset:0
	ds_read_b128 v[248:251], v182 offset:0
	s_waitcnt lgkmcnt(6)
	v_mfma_f32_32x32x16_bf16 v[0:15], v[202:205], v[136:139], v[0:15]
	ds_read_b128 v[218:221], v182 offset:0x2000
	ds_read_b128 v[222:225], v180 offset:0x400
	s_waitcnt lgkmcnt(6)
	v_mfma_f32_32x32x16_bf16 v[0:15], v[206:209], v[140:143], v[0:15]
	s_waitcnt lgkmcnt(3)
	s_nop 0
	v_mfma_f32_32x32x16_bf16 v[144:159], v[236:239], v[244:247], 0
	ds_read_b128 v[194:197], v183 offset:0
	ds_read_b128 v[198:201], v183 offset:0x2000
	v_mfma_f32_32x32x16_bf16 v[128:143], v[240:243], v[244:247], 0
	ds_read_b128 v[202:205], v180 offset:0x800
	s_waitcnt lgkmcnt(3)
	v_mfma_f32_32x32x16_bf16 v[144:159], v[248:251], v[222:225], v[144:159]
	ds_read_b128 v[236:239], v184 offset:0
	ds_read_b128 v[240:243], v184 offset:0x2000
	v_mfma_f32_32x32x16_bf16 v[128:143], v[218:221], v[222:225], v[128:143]
	ds_read_b128 v[244:247], v180 offset:0xc00
	s_waitcnt lgkmcnt(3)
	v_mfma_f32_32x32x16_bf16 v[144:159], v[194:197], v[202:205], v[144:159]
	ds_read_b128 v[248:251], v181 offset:0x80
	ds_read_b128 v[218:221], v181 offset:0x2080
	v_mfma_f32_32x32x16_bf16 v[128:143], v[198:201], v[202:205], v[128:143]
	ds_read_b128 v[222:225], v180 offset:0x1000
	s_waitcnt lgkmcnt(3)
	v_mfma_f32_32x32x16_bf16 v[144:159], v[236:239], v[244:247], v[144:159]
	ds_read_b128 v[194:197], v182 offset:0x80
	ds_read_b128 v[198:201], v182 offset:0x2080
	v_mfma_f32_32x32x16_bf16 v[128:143], v[240:243], v[244:247], v[128:143]
	ds_read_b128 v[202:205], v180 offset:0x1400
	s_waitcnt lgkmcnt(3)
	v_mfma_f32_32x32x16_bf16 v[144:159], v[248:251], v[222:225], v[144:159]
	ds_read_b128 v[236:239], v183 offset:0x80
	ds_read_b128 v[240:243], v183 offset:0x2080
	v_mfma_f32_32x32x16_bf16 v[128:143], v[218:221], v[222:225], v[128:143]
	ds_read_b128 v[244:247], v180 offset:0x1800
	s_waitcnt lgkmcnt(3)
	v_mfma_f32_32x32x16_bf16 v[144:159], v[194:197], v[202:205], v[144:159]
	ds_read_b128 v[248:251], v184 offset:0x80
	ds_read_b128 v[218:221], v184 offset:0x2080
	v_mfma_f32_32x32x16_bf16 v[128:143], v[198:201], v[202:205], v[128:143]
	s_waitcnt lgkmcnt(2)
	v_mfma_f32_32x32x16_bf16 v[144:159], v[236:239], v[244:247], v[144:159]
	v_mfma_f32_32x32x16_bf16 v[128:143], v[240:243], v[244:247], v[128:143]
	s_waitcnt lgkmcnt(0)
	v_mfma_f32_32x32x16_bf16 v[144:159], v[248:251], v[166:169], v[144:159]
	v_mfma_f32_32x32x16_bf16 v[128:143], v[218:221], v[166:169], v[128:143]
	s_bitcmp0_b32 s100, 8
	s_cbranch_scc1 .Lstg_a11
	s_waitcnt vmcnt(0)
	s_waitcnt lgkmcnt(0)
	s_barrier
	s_sleep 5

.LBB0_580:
	ds_read_b64_tr_b16 v[144:145], v177 offset:0
	ds_read_b64_tr_b16 v[146:147], v177 offset:0x1000
	ds_read_b64_tr_b16 v[148:149], v177 offset:0x2000
	ds_read_b64_tr_b16 v[150:151], v177 offset:0x3000
	ds_read_b64_tr_b16 v[152:153], v177 offset:0x4000
	ds_read_b64_tr_b16 v[154:155], v177 offset:0x5000
	ds_read_b64_tr_b16 v[156:157], v177 offset:0x6000
	ds_read_b64_tr_b16 v[158:159], v177 offset:0x7000
	s_waitcnt lgkmcnt(6)
	s_nop 0
	v_mfma_f32_32x32x16_bf16 v[112:127], v[144:147], v[128:131], v[112:127]
	ds_read_b64_tr_b16 v[192:193], v177 offset:0x200
	ds_read_b64_tr_b16 v[194:195], v177 offset:0x1200
	s_waitcnt lgkmcnt(6)
	v_mfma_f32_32x32x16_bf16 v[112:127], v[148:151], v[132:135], v[112:127]
	ds_read_b64_tr_b16 v[196:197], v177 offset:0x2200
	ds_read_b64_tr_b16 v[198:199], v177 offset:0x3200
	s_waitcnt lgkmcnt(6)
	v_mfma_f32_32x32x16_bf16 v[112:127], v[152:155], v[136:139], v[112:127]
	ds_read_b64_tr_b16 v[200:201], v177 offset:0x4200
	ds_read_b64_tr_b16 v[202:203], v177 offset:0x5200
	s_waitcnt lgkmcnt(6)
	v_mfma_f32_32x32x16_bf16 v[112:127], v[156:159], v[140:143], v[112:127]
	ds_read_b64_tr_b16 v[204:205], v177 offset:0x6200
	ds_read_b64_tr_b16 v[206:207], v177 offset:0x7200
	s_waitcnt lgkmcnt(6)
	v_mfma_f32_32x32x16_bf16 v[80:95], v[192:195], v[128:131], v[80:95]
	ds_read_b64_tr_b16 v[144:145], v177 offset:0x400
	ds_read_b64_tr_b16 v[146:147], v177 offset:0x1400
	s_waitcnt lgkmcnt(6)
	v_mfma_f32_32x32x16_bf16 v[80:95], v[196:199], v[132:135], v[80:95]
	ds_read_b64_tr_b16 v[148:149], v177 offset:0x2400
	ds_read_b64_tr_b16 v[150:151], v177 offset:0x3400
	s_waitcnt lgkmcnt(6)
	v_mfma_f32_32x32x16_bf16 v[80:95], v[200:203], v[136:139], v[80:95]
	ds_read_b64_tr_b16 v[152:153], v177 offset:0x4400
	ds_read_b64_tr_b16 v[154:155], v177 offset:0x5400
	s_waitcnt lgkmcnt(6)
	v_mfma_f32_32x32x16_bf16 v[80:95], v[204:207], v[140:143], v[80:95]
	ds_read_b64_tr_b16 v[156:157], v177 offset:0x6400
	ds_read_b64_tr_b16 v[158:159], v177 offset:0x7400
	s_waitcnt lgkmcnt(6)
	v_mfma_f32_32x32x16_bf16 v[96:111], v[144:147], v[128:131], v[96:111]
	ds_read_b64_tr_b16 v[192:193], v177 offset:0x600
	ds_read_b64_tr_b16 v[194:195], v177 offset:0x1600
	s_waitcnt lgkmcnt(6)
	v_mfma_f32_32x32x16_bf16 v[96:111], v[148:151], v[132:135], v[96:111]
	ds_read_b64_tr_b16 v[196:197], v177 offset:0x2600
	ds_read_b64_tr_b16 v[198:199], v177 offset:0x3600
	s_waitcnt lgkmcnt(6)
	v_mfma_f32_32x32x16_bf16 v[96:111], v[152:155], v[136:139], v[96:111]
	ds_read_b64_tr_b16 v[200:201], v177 offset:0x4600
	ds_read_b64_tr_b16 v[202:203], v177 offset:0x5600
	s_waitcnt lgkmcnt(6)
	v_mfma_f32_32x32x16_bf16 v[96:111], v[156:159], v[140:143], v[96:111]
	ds_read_b64_tr_b16 v[204:205], v177 offset:0x6600
	ds_read_b64_tr_b16 v[206:207], v177 offset:0x7600
	s_waitcnt lgkmcnt(6)
	v_mfma_f32_32x32x16_bf16 v[64:79], v[192:195], v[128:131], v[64:79]
	ds_read_b64_tr_b16 v[144:145], v177 offset:0x800
	ds_read_b64_tr_b16 v[146:147], v177 offset:0x1800
	s_waitcnt lgkmcnt(6)
	v_mfma_f32_32x32x16_bf16 v[64:79], v[196:199], v[132:135], v[64:79]
	ds_read_b64_tr_b16 v[148:149], v177 offset:0x2800
	ds_read_b64_tr_b16 v[150:151], v177 offset:0x3800
	s_waitcnt lgkmcnt(6)
	v_mfma_f32_32x32x16_bf16 v[64:79], v[200:203], v[136:139], v[64:79]
	ds_read_b64_tr_b16 v[152:153], v177 offset:0x4800
	ds_read_b64_tr_b16 v[154:155], v177 offset:0x5800
	s_waitcnt lgkmcnt(6)
	v_mfma_f32_32x32x16_bf16 v[64:79], v[204:207], v[140:143], v[64:79]
	ds_read_b64_tr_b16 v[156:157], v177 offset:0x6800
	ds_read_b64_tr_b16 v[158:159], v177 offset:0x7800
	s_waitcnt lgkmcnt(6)
	v_mfma_f32_32x32x16_bf16 v[48:63], v[144:147], v[128:131], v[48:63]
	ds_read_b64_tr_b16 v[192:193], v177 offset:0xa00
	ds_read_b64_tr_b16 v[194:195], v177 offset:0x1a00
	s_waitcnt lgkmcnt(6)
	v_mfma_f32_32x32x16_bf16 v[48:63], v[148:151], v[132:135], v[48:63]
	ds_read_b64_tr_b16 v[196:197], v177 offset:0x2a00
	ds_read_b64_tr_b16 v[198:199], v177 offset:0x3a00
	s_waitcnt lgkmcnt(6)
	v_mfma_f32_32x32x16_bf16 v[48:63], v[152:155], v[136:139], v[48:63]
	ds_read_b64_tr_b16 v[200:201], v177 offset:0x4a00
	ds_read_b64_tr_b16 v[202:203], v177 offset:0x5a00
	s_waitcnt lgkmcnt(6)
	v_mfma_f32_32x32x16_bf16 v[48:63], v[156:159], v[140:143], v[48:63]
	ds_read_b64_tr_b16 v[204:205], v177 offset:0x6a00
	ds_read_b64_tr_b16 v[206:207], v177 offset:0x7a00
	s_waitcnt lgkmcnt(6)
	v_mfma_f32_32x32x16_bf16 v[32:47], v[192:195], v[128:131], v[32:47]
	ds_read_b64_tr_b16 v[144:145], v177 offset:0xc00
	ds_read_b64_tr_b16 v[146:147], v177 offset:0x1c00
	s_waitcnt lgkmcnt(6)
	v_mfma_f32_32x32x16_bf16 v[32:47], v[196:199], v[132:135], v[32:47]
	ds_read_b64_tr_b16 v[148:149], v177 offset:0x2c00
	ds_read_b64_tr_b16 v[150:151], v177 offset:0x3c00
	s_waitcnt lgkmcnt(6)
	v_mfma_f32_32x32x16_bf16 v[32:47], v[200:203], v[136:139], v[32:47]
	ds_read_b64_tr_b16 v[152:153], v177 offset:0x4c00
	ds_read_b64_tr_b16 v[154:155], v177 offset:0x5c00
	s_waitcnt lgkmcnt(6)
	v_mfma_f32_32x32x16_bf16 v[32:47], v[204:207], v[140:143], v[32:47]
	ds_read_b64_tr_b16 v[156:157], v177 offset:0x6c00
	ds_read_b64_tr_b16 v[158:159], v177 offset:0x7c00
	s_waitcnt lgkmcnt(6)
	v_mfma_f32_32x32x16_bf16 v[16:31], v[144:147], v[128:131], v[16:31]
	ds_read_b64_tr_b16 v[192:193], v177 offset:0xe00
	ds_read_b64_tr_b16 v[194:195], v177 offset:0x1e00
	s_waitcnt lgkmcnt(6)
	v_mfma_f32_32x32x16_bf16 v[16:31], v[148:151], v[132:135], v[16:31]
	ds_read_b64_tr_b16 v[196:197], v177 offset:0x2e00
	ds_read_b64_tr_b16 v[198:199], v177 offset:0x3e00
	s_waitcnt lgkmcnt(6)
	v_mfma_f32_32x32x16_bf16 v[16:31], v[152:155], v[136:139], v[16:31]
	ds_read_b64_tr_b16 v[200:201], v177 offset:0x4e00
	ds_read_b64_tr_b16 v[202:203], v177 offset:0x5e00
	s_waitcnt lgkmcnt(6)
	v_mfma_f32_32x32x16_bf16 v[16:31], v[156:159], v[140:143], v[16:31]
	ds_read_b64_tr_b16 v[204:205], v177 offset:0x6e00
	ds_read_b64_tr_b16 v[206:207], v177 offset:0x7e00
	s_waitcnt lgkmcnt(6)
	v_mfma_f32_32x32x16_bf16 v[0:15], v[192:195], v[128:131], v[0:15]
	s_waitcnt lgkmcnt(4)
	v_mfma_f32_32x32x16_bf16 v[0:15], v[196:199], v[132:135], v[0:15]
	s_waitcnt lgkmcnt(2)
	v_mfma_f32_32x32x16_bf16 v[0:15], v[200:203], v[136:139], v[0:15]
	s_waitcnt lgkmcnt(0)
	v_mfma_f32_32x32x16_bf16 v[0:15], v[204:207], v[140:143], v[0:15]
	ds_read_b128 v[128:131], v188 offset:0
	ds_read_b128 v[132:135], v188 offset:0x2000
	ds_read_b128 v[136:139], v180 offset:0
	ds_read_b128 v[192:195], v187 offset:0
	ds_read_b128 v[196:199], v187 offset:0x2000
	ds_read_b128 v[200:203], v180 offset:0x400
	s_waitcnt lgkmcnt(3)
	s_nop 0
	v_mfma_f32_32x32x16_bf16 v[144:159], v[128:131], v[136:139], 0
	v_mfma_f32_32x32x16_bf16 v[128:143], v[132:135], v[136:139], 0
	ds_read_b128 v[204:207], v186 offset:0
	ds_read_b128 v[208:211], v186 offset:0x2000
	ds_read_b128 v[212:215], v180 offset:0x800
	s_waitcnt lgkmcnt(3)
	v_mfma_f32_32x32x16_bf16 v[144:159], v[192:195], v[200:203], v[144:159]
	v_mfma_f32_32x32x16_bf16 v[128:143], v[196:199], v[200:203], v[128:143]
	ds_read_b128 v[192:195], v185 offset:0
	ds_read_b128 v[196:199], v185 offset:0x2000
	ds_read_b128 v[200:203], v180 offset:0xc00
	s_waitcnt lgkmcnt(3)
	v_mfma_f32_32x32x16_bf16 v[144:159], v[204:207], v[212:215], v[144:159]
	v_mfma_f32_32x32x16_bf16 v[128:143], v[208:211], v[212:215], v[128:143]
	ds_read_b128 v[204:207], v188 offset:0x80
	ds_read_b128 v[208:211], v188 offset:0x2080
	ds_read_b128 v[212:215], v180 offset:0x1000
	s_waitcnt lgkmcnt(3)
	v_mfma_f32_32x32x16_bf16 v[144:159], v[192:195], v[200:203], v[144:159]
	v_mfma_f32_32x32x16_bf16 v[128:143], v[196:199], v[200:203], v[128:143]
	ds_read_b128 v[192:195], v187 offset:0x80
	ds_read_b128 v[196:199], v187 offset:0x2080
	ds_read_b128 v[200:203], v180 offset:0x1400
	s_waitcnt lgkmcnt(3)
	v_mfma_f32_32x32x16_bf16 v[144:159], v[204:207], v[212:215], v[144:159]
	v_mfma_f32_32x32x16_bf16 v[128:143], v[208:211], v[212:215], v[128:143]
	ds_read_b128 v[204:207], v186 offset:0x80
	ds_read_b128 v[208:211], v186 offset:0x2080
	ds_read_b128 v[186:189], v180 offset:0x1800
	s_waitcnt lgkmcnt(3)
	v_mfma_f32_32x32x16_bf16 v[144:159], v[192:195], v[200:203], v[144:159]
	v_mfma_f32_32x32x16_bf16 v[128:143], v[196:199], v[200:203], v[128:143]
	ds_read_b128 v[180:183], v185 offset:0x80
	ds_read_b128 v[192:195], v185 offset:0x2080
	s_waitcnt lgkmcnt(2)
	v_mfma_f32_32x32x16_bf16 v[144:159], v[204:207], v[186:189], v[144:159]
	v_mfma_f32_32x32x16_bf16 v[128:143], v[208:211], v[186:189], v[128:143]
	s_waitcnt lgkmcnt(0)
	v_mfma_f32_32x32x16_bf16 v[144:159], v[180:183], v[166:169], v[144:159]
	v_mfma_f32_32x32x16_bf16 v[128:143], v[192:195], v[166:169], v[128:143]
	s_bitcmp0_b32 s100, 8
	s_cbranch_scc1 .Lstg_a12
	s_waitcnt vmcnt(0)
	s_waitcnt lgkmcnt(0)
	s_barrier
	s_sleep 5

.LBB0_586:
	s_or_b64 exec, exec, s[4:5]
	v_mov_b32_e32 v38, v165
	v_readlane_b32 s5, v255, 51
	v_readfirstlane_b32 s2, v38
	s_ashr_i32 s79, s2, 6
	v_bfe_u32 v0, v38, 5, 1
	v_and_b32_e32 v176, 31, v38
	s_lshl_b32 s92, s79, 5
	v_lshlrev_b32_e32 v32, 2, v0
	s_add_i32 s74, s92, s74
	v_sub_u32_e32 v1, v176, v32
	v_lshlrev_b32_e32 v175, 4, v0
	s_lshl_b32 s2, s79, 3
	v_bfe_u32 v0, v38, 4, 2
	v_add_u32_e32 v179, s74, v1
	v_or_b32_e32 v1, s2, v0
	v_and_b32_e32 v2, 15, v38
	v_and_b32_e32 v39, 63, v38
	v_bitop3_b32 v3, v0, v38, 15 bitop3:0x78
	v_mul_lo_u32 v1, v1, s14
	v_bitop3_b32 v0, v0, v2, 4 bitop3:0x36
	s_mul_i32 s4, s79, 0x1c00
	s_waitcnt vmcnt(16)
	v_lshlrev_b32_e32 v40, 4, v39
	v_lshl_or_b32 v0, v0, 4, v1
	s_lshl_b32 s78, s79, 11
	v_readlane_b32 s7, v255, 53
	s_lshl_b32 s3, s79, 12
	s_add_i32 s4, s5, s4
	v_lshl_or_b32 v160, v3, 4, v1
	v_add_u32_e32 v170, 0x1a000, v0
	s_add_i32 s78, s78, s7
	s_add_i32 s3, s3, s33
	v_add_u32_e32 v180, s4, v40
	s_waitcnt vmcnt(16) lgkmcnt(0)
	ds_write_b128 v180, v[128:131]
	ds_write_b128 v180, v[132:135] offset:1024
	ds_write_b128 v180, v[136:139] offset:2048
	ds_write_b128 v180, v[140:143] offset:3072
	ds_write_b128 v180, v[144:147] offset:4096
	ds_write_b128 v180, v[148:151] offset:5120
	ds_write_b128 v180, v[152:155] offset:6144
	s_add_u32 s4, s66, 0x1a2900
	s_addc_u32 s5, s67, 0
	v_lshl_add_u64 v[0:1], s[4:5], 0, v[160:161]
	s_add_i32 s82, s78, 0x4000
	s_mov_b32 s6, m0
	s_mov_b32 m0, s82
	s_nop 0
	global_load_lds_dwordx4 v[0:1], off
	s_mov_b32 m0, s6
	v_mov_b32_e32 v171, v161
	v_lshl_add_u64 v[0:1], s[4:5], 0, v[170:171]
	s_add_i32 s84, s78, 0x4400
	s_mov_b32 s4, m0
	s_mov_b32 m0, s84
	s_nop 0
	global_load_lds_dwordx4 v[0:1], off
	s_mov_b32 m0, s4
	s_waitcnt lgkmcnt(0)
	s_barrier
	v_lshlrev_b32_e32 v0, 4, v38
	s_movk_i32 s4, 0x70
	v_lshlrev_b32_e32 v33, 8, v176
	v_and_b32_e32 v1, 0x70, v0
	v_bitop3_b32 v34, v175, v0, s4 bitop3:0x78
	s_movk_i32 s4, 0x60
	v_add_u32_e32 v2, s7, v33
	v_bitop3_b32 v35, v175, v1, 32 bitop3:0x36
	v_bitop3_b32 v36, v175, v1, 64 bitop3:0x36
	v_bitop3_b32 v37, v175, v1, s4 bitop3:0x36
	v_add_u32_e32 v181, v34, v2
	v_add_u32_e32 v182, v35, v2
	v_add_u32_e32 v183, v36, v2
	v_add_u32_e32 v184, v37, v2
	ds_read_b128 v[0:3], v181 offset:0
	ds_read_b128 v[4:7], v181 offset:0x2000
	ds_read_b128 v[8:11], v180 offset:0
	ds_read_b128 v[42:45], v182 offset:0
	ds_read_b128 v[46:49], v182 offset:0x2000
	ds_read_b128 v[50:53], v180 offset:0x400
	s_waitcnt lgkmcnt(3)
	s_nop 0
	v_mfma_f32_32x32x16_bf16 v[16:31], v[0:3], v[8:11], 0
	v_mfma_f32_32x32x16_bf16 v[0:15], v[4:7], v[8:11], 0
	ds_read_b128 v[54:57], v183 offset:0
	ds_read_b128 v[58:61], v183 offset:0x2000
	ds_read_b128 v[62:65], v180 offset:0x800
	s_waitcnt lgkmcnt(3)
	v_mfma_f32_32x32x16_bf16 v[16:31], v[42:45], v[50:53], v[16:31]
	v_mfma_f32_32x32x16_bf16 v[0:15], v[46:49], v[50:53], v[0:15]
	ds_read_b128 v[42:45], v184 offset:0
	ds_read_b128 v[46:49], v184 offset:0x2000
	ds_read_b128 v[50:53], v180 offset:0xc00
	s_waitcnt lgkmcnt(3)
	v_mfma_f32_32x32x16_bf16 v[16:31], v[54:57], v[62:65], v[16:31]
	v_mfma_f32_32x32x16_bf16 v[0:15], v[58:61], v[62:65], v[0:15]
	ds_read_b128 v[54:57], v181 offset:0x80
	ds_read_b128 v[58:61], v181 offset:0x2080
	ds_read_b128 v[62:65], v180 offset:0x1000
	s_waitcnt lgkmcnt(3)
	v_mfma_f32_32x32x16_bf16 v[16:31], v[42:45], v[50:53], v[16:31]
	v_mfma_f32_32x32x16_bf16 v[0:15], v[46:49], v[50:53], v[0:15]
	ds_read_b128 v[42:45], v182 offset:0x80
	ds_read_b128 v[46:49], v182 offset:0x2080
	ds_read_b128 v[50:53], v180 offset:0x1400
	s_waitcnt lgkmcnt(3)
	v_mfma_f32_32x32x16_bf16 v[16:31], v[54:57], v[62:65], v[16:31]
	v_mfma_f32_32x32x16_bf16 v[0:15], v[58:61], v[62:65], v[0:15]
	ds_read_b128 v[54:57], v183 offset:0x80
	ds_read_b128 v[58:61], v183 offset:0x2080
	ds_read_b128 v[62:65], v180 offset:0x1800
	s_waitcnt lgkmcnt(3)
	v_mfma_f32_32x32x16_bf16 v[16:31], v[42:45], v[50:53], v[16:31]
	v_mfma_f32_32x32x16_bf16 v[0:15], v[46:49], v[50:53], v[0:15]
	ds_read_b128 v[42:45], v184 offset:0x80
	ds_read_b128 v[46:49], v184 offset:0x2080
	s_waitcnt lgkmcnt(2)
	v_mfma_f32_32x32x16_bf16 v[16:31], v[54:57], v[62:65], v[16:31]
	v_mfma_f32_32x32x16_bf16 v[0:15], v[58:61], v[62:65], v[0:15]
	s_waitcnt lgkmcnt(0)
	v_mfma_f32_32x32x16_bf16 v[16:31], v[42:45], v[166:169], v[16:31]
	v_mfma_f32_32x32x16_bf16 v[0:15], v[46:49], v[166:169], v[0:15]
	s_bitcmp0_b32 s100, 8
	s_cbranch_scc1 .Lstg_a17
	s_waitcnt vmcnt(0)
	s_waitcnt lgkmcnt(0)
	s_barrier
	s_sleep 5

.LBB0_589:
	ds_read_b64_tr_b16 v[144:145], v177 offset:0
	ds_read_b64_tr_b16 v[146:147], v177 offset:0x1000
	ds_read_b64_tr_b16 v[148:149], v177 offset:0x2000
	ds_read_b64_tr_b16 v[150:151], v177 offset:0x3000
	ds_read_b64_tr_b16 v[152:153], v177 offset:0x4000
	ds_read_b64_tr_b16 v[154:155], v177 offset:0x5000
	ds_read_b64_tr_b16 v[156:157], v177 offset:0x6000
	ds_read_b64_tr_b16 v[158:159], v177 offset:0x7000
	s_waitcnt lgkmcnt(6)
	s_nop 0
	v_mfma_f32_32x32x16_bf16 v[112:127], v[144:147], v[128:131], v[112:127]
	ds_read_b64_tr_b16 v[192:193], v177 offset:0x200
	ds_read_b64_tr_b16 v[194:195], v177 offset:0x1200
	s_waitcnt lgkmcnt(6)
	v_mfma_f32_32x32x16_bf16 v[112:127], v[148:151], v[132:135], v[112:127]
	ds_read_b64_tr_b16 v[196:197], v177 offset:0x2200
	ds_read_b64_tr_b16 v[198:199], v177 offset:0x3200
	s_waitcnt lgkmcnt(6)
	v_mfma_f32_32x32x16_bf16 v[112:127], v[152:155], v[136:139], v[112:127]
	ds_read_b64_tr_b16 v[200:201], v177 offset:0x4200
	ds_read_b64_tr_b16 v[202:203], v177 offset:0x5200
	s_waitcnt lgkmcnt(6)
	v_mfma_f32_32x32x16_bf16 v[112:127], v[156:159], v[140:143], v[112:127]
	ds_read_b64_tr_b16 v[204:205], v177 offset:0x6200
	ds_read_b64_tr_b16 v[206:207], v177 offset:0x7200
	s_waitcnt lgkmcnt(6)
	v_mfma_f32_32x32x16_bf16 v[96:111], v[192:195], v[128:131], v[96:111]
	ds_read_b64_tr_b16 v[144:145], v177 offset:0x400
	ds_read_b64_tr_b16 v[146:147], v177 offset:0x1400
	s_waitcnt lgkmcnt(6)
	v_mfma_f32_32x32x16_bf16 v[96:111], v[196:199], v[132:135], v[96:111]
	ds_read_b64_tr_b16 v[148:149], v177 offset:0x2400
	ds_read_b64_tr_b16 v[150:151], v177 offset:0x3400
	s_waitcnt lgkmcnt(6)
	v_mfma_f32_32x32x16_bf16 v[96:111], v[200:203], v[136:139], v[96:111]
	ds_read_b64_tr_b16 v[152:153], v177 offset:0x4400
	ds_read_b64_tr_b16 v[154:155], v177 offset:0x5400
	s_waitcnt lgkmcnt(6)
	v_mfma_f32_32x32x16_bf16 v[96:111], v[204:207], v[140:143], v[96:111]
	ds_read_b64_tr_b16 v[156:157], v177 offset:0x6400
	ds_read_b64_tr_b16 v[158:159], v177 offset:0x7400
	s_waitcnt lgkmcnt(6)
	v_mfma_f32_32x32x16_bf16 v[80:95], v[144:147], v[128:131], v[80:95]
	ds_read_b64_tr_b16 v[192:193], v177 offset:0x600
	ds_read_b64_tr_b16 v[194:195], v177 offset:0x1600
	s_waitcnt lgkmcnt(6)
	v_mfma_f32_32x32x16_bf16 v[80:95], v[148:151], v[132:135], v[80:95]
	ds_read_b64_tr_b16 v[196:197], v177 offset:0x2600
	ds_read_b64_tr_b16 v[198:199], v177 offset:0x3600
	s_waitcnt lgkmcnt(6)
	v_mfma_f32_32x32x16_bf16 v[80:95], v[152:155], v[136:139], v[80:95]
	ds_read_b64_tr_b16 v[200:201], v177 offset:0x4600
	ds_read_b64_tr_b16 v[202:203], v177 offset:0x5600
	s_waitcnt lgkmcnt(6)
	v_mfma_f32_32x32x16_bf16 v[80:95], v[156:159], v[140:143], v[80:95]
	ds_read_b64_tr_b16 v[204:205], v177 offset:0x6600
	ds_read_b64_tr_b16 v[206:207], v177 offset:0x7600
	s_waitcnt lgkmcnt(6)
	v_mfma_f32_32x32x16_bf16 v[64:79], v[192:195], v[128:131], v[64:79]
	ds_read_b64_tr_b16 v[144:145], v177 offset:0x800
	ds_read_b64_tr_b16 v[146:147], v177 offset:0x1800
	s_waitcnt lgkmcnt(6)
	v_mfma_f32_32x32x16_bf16 v[64:79], v[196:199], v[132:135], v[64:79]
	ds_read_b64_tr_b16 v[148:149], v177 offset:0x2800
	ds_read_b64_tr_b16 v[150:151], v177 offset:0x3800
	s_waitcnt lgkmcnt(6)
	v_mfma_f32_32x32x16_bf16 v[64:79], v[200:203], v[136:139], v[64:79]
	ds_read_b64_tr_b16 v[152:153], v177 offset:0x4800
	ds_read_b64_tr_b16 v[154:155], v177 offset:0x5800
	s_waitcnt lgkmcnt(6)
	v_mfma_f32_32x32x16_bf16 v[64:79], v[204:207], v[140:143], v[64:79]
	ds_read_b64_tr_b16 v[156:157], v177 offset:0x6800
	ds_read_b64_tr_b16 v[158:159], v177 offset:0x7800
	s_waitcnt lgkmcnt(6)
	v_mfma_f32_32x32x16_bf16 v[48:63], v[144:147], v[128:131], v[48:63]
	ds_read_b64_tr_b16 v[192:193], v177 offset:0xa00
	ds_read_b64_tr_b16 v[194:195], v177 offset:0x1a00
	s_waitcnt lgkmcnt(6)
	v_mfma_f32_32x32x16_bf16 v[48:63], v[148:151], v[132:135], v[48:63]
	ds_read_b64_tr_b16 v[196:197], v177 offset:0x2a00
	ds_read_b64_tr_b16 v[198:199], v177 offset:0x3a00
	s_waitcnt lgkmcnt(6)
	v_mfma_f32_32x32x16_bf16 v[48:63], v[152:155], v[136:139], v[48:63]
	ds_read_b64_tr_b16 v[200:201], v177 offset:0x4a00
	ds_read_b64_tr_b16 v[202:203], v177 offset:0x5a00
	s_waitcnt lgkmcnt(6)
	v_mfma_f32_32x32x16_bf16 v[48:63], v[156:159], v[140:143], v[48:63]
	ds_read_b64_tr_b16 v[204:205], v177 offset:0x6a00
	ds_read_b64_tr_b16 v[206:207], v177 offset:0x7a00
	s_waitcnt lgkmcnt(6)
	v_mfma_f32_32x32x16_bf16 v[32:47], v[192:195], v[128:131], v[32:47]
	ds_read_b64_tr_b16 v[144:145], v177 offset:0xc00
	ds_read_b64_tr_b16 v[146:147], v177 offset:0x1c00
	s_waitcnt lgkmcnt(6)
	v_mfma_f32_32x32x16_bf16 v[32:47], v[196:199], v[132:135], v[32:47]
	ds_read_b64_tr_b16 v[148:149], v177 offset:0x2c00
	ds_read_b64_tr_b16 v[150:151], v177 offset:0x3c00
	s_waitcnt lgkmcnt(6)
	v_mfma_f32_32x32x16_bf16 v[32:47], v[200:203], v[136:139], v[32:47]
	ds_read_b64_tr_b16 v[152:153], v177 offset:0x4c00
	ds_read_b64_tr_b16 v[154:155], v177 offset:0x5c00
	s_waitcnt lgkmcnt(6)
	v_mfma_f32_32x32x16_bf16 v[32:47], v[204:207], v[140:143], v[32:47]
	ds_read_b64_tr_b16 v[156:157], v177 offset:0x6c00
	ds_read_b64_tr_b16 v[158:159], v177 offset:0x7c00
	s_waitcnt lgkmcnt(6)
	v_mfma_f32_32x32x16_bf16 v[16:31], v[144:147], v[128:131], v[16:31]
	ds_read_b64_tr_b16 v[192:193], v177 offset:0xe00
	ds_read_b64_tr_b16 v[194:195], v177 offset:0x1e00
	s_waitcnt lgkmcnt(6)
	v_mfma_f32_32x32x16_bf16 v[16:31], v[148:151], v[132:135], v[16:31]
	ds_read_b64_tr_b16 v[196:197], v177 offset:0x2e00
	ds_read_b64_tr_b16 v[198:199], v177 offset:0x3e00
	s_waitcnt lgkmcnt(6)
	v_mfma_f32_32x32x16_bf16 v[16:31], v[152:155], v[136:139], v[16:31]
	ds_read_b64_tr_b16 v[200:201], v177 offset:0x4e00
	ds_read_b64_tr_b16 v[202:203], v177 offset:0x5e00
	s_waitcnt lgkmcnt(6)
	v_mfma_f32_32x32x16_bf16 v[16:31], v[156:159], v[140:143], v[16:31]
	ds_read_b64_tr_b16 v[204:205], v177 offset:0x6e00
	ds_read_b64_tr_b16 v[206:207], v177 offset:0x7e00
	s_waitcnt lgkmcnt(6)
	v_mfma_f32_32x32x16_bf16 v[0:15], v[192:195], v[128:131], v[0:15]
	ds_read_b128 v[236:239], v188 offset:0
	ds_read_b128 v[240:243], v188 offset:0x2000
	s_waitcnt lgkmcnt(6)
	v_mfma_f32_32x32x16_bf16 v[0:15], v[196:199], v[132:135], v[0:15]
	ds_read_b128 v[244:247], v180 offset:0
	ds_read_b128 v[248:251], v187 offset:0
	s_waitcnt lgkmcnt(6)
	v_mfma_f32_32x32x16_bf16 v[0:15], v[200:203], v[136:139], v[0:15]
	ds_read_b128 v[218:221], v187 offset:0x2000
	ds_read_b128 v[222:225], v180 offset:0x400
	s_waitcnt lgkmcnt(6)
	v_mfma_f32_32x32x16_bf16 v[0:15], v[204:207], v[140:143], v[0:15]
	s_waitcnt lgkmcnt(3)
	s_nop 0
	v_mfma_f32_32x32x16_bf16 v[144:159], v[236:239], v[244:247], 0
	ds_read_b128 v[192:195], v186 offset:0
	ds_read_b128 v[196:199], v186 offset:0x2000
	v_mfma_f32_32x32x16_bf16 v[128:143], v[240:243], v[244:247], 0
	ds_read_b128 v[200:203], v180 offset:0x800
	s_waitcnt lgkmcnt(3)
	v_mfma_f32_32x32x16_bf16 v[144:159], v[248:251], v[222:225], v[144:159]
	ds_read_b128 v[236:239], v185 offset:0
	ds_read_b128 v[240:243], v185 offset:0x2000
	v_mfma_f32_32x32x16_bf16 v[128:143], v[218:221], v[222:225], v[128:143]
	ds_read_b128 v[244:247], v180 offset:0xc00
	s_waitcnt lgkmcnt(3)
	v_mfma_f32_32x32x16_bf16 v[144:159], v[192:195], v[200:203], v[144:159]
	ds_read_b128 v[248:251], v188 offset:0x80
	ds_read_b128 v[218:221], v188 offset:0x2080
	v_mfma_f32_32x32x16_bf16 v[128:143], v[196:199], v[200:203], v[128:143]
	ds_read_b128 v[222:225], v180 offset:0x1000
	s_waitcnt lgkmcnt(3)
	v_mfma_f32_32x32x16_bf16 v[144:159], v[236:239], v[244:247], v[144:159]
	ds_read_b128 v[192:195], v187 offset:0x80
	ds_read_b128 v[196:199], v187 offset:0x2080
	v_mfma_f32_32x32x16_bf16 v[128:143], v[240:243], v[244:247], v[128:143]
	ds_read_b128 v[200:203], v180 offset:0x1400
	s_waitcnt lgkmcnt(3)
	v_mfma_f32_32x32x16_bf16 v[144:159], v[248:251], v[222:225], v[144:159]
	ds_read_b128 v[236:239], v186 offset:0x80
	ds_read_b128 v[240:243], v186 offset:0x2080
	v_mfma_f32_32x32x16_bf16 v[128:143], v[218:221], v[222:225], v[128:143]
	ds_read_b128 v[244:247], v180 offset:0x1800
	s_waitcnt lgkmcnt(3)
	v_mfma_f32_32x32x16_bf16 v[144:159], v[192:195], v[200:203], v[144:159]
	ds_read_b128 v[248:251], v185 offset:0x80
	ds_read_b128 v[218:221], v185 offset:0x2080
	v_mfma_f32_32x32x16_bf16 v[128:143], v[196:199], v[200:203], v[128:143]
	s_waitcnt lgkmcnt(2)
	v_mfma_f32_32x32x16_bf16 v[144:159], v[236:239], v[244:247], v[144:159]
	v_mfma_f32_32x32x16_bf16 v[128:143], v[240:243], v[244:247], v[128:143]
	s_waitcnt lgkmcnt(0)
	v_mfma_f32_32x32x16_bf16 v[144:159], v[248:251], v[166:169], v[144:159]
	v_mfma_f32_32x32x16_bf16 v[128:143], v[218:221], v[166:169], v[128:143]
	s_bitcmp0_b32 s100, 8
	s_cbranch_scc1 .Lstg_a18
	s_waitcnt vmcnt(0)
	s_waitcnt lgkmcnt(0)
	s_barrier
	s_sleep 5

.LBB0_597:
	ds_read_b64_tr_b16 v[144:145], v177 offset:0x8000
	ds_read_b64_tr_b16 v[146:147], v177 offset:0x9000
	ds_read_b64_tr_b16 v[148:149], v177 offset:0xa000
	ds_read_b64_tr_b16 v[150:151], v177 offset:0xb000
	ds_read_b64_tr_b16 v[152:153], v177 offset:0xc000
	ds_read_b64_tr_b16 v[154:155], v177 offset:0xd000
	ds_read_b64_tr_b16 v[156:157], v177 offset:0xe000
	ds_read_b64_tr_b16 v[158:159], v177 offset:0xf000
	s_waitcnt lgkmcnt(6)
	s_nop 0
	v_mfma_f32_32x32x16_bf16 v[112:127], v[144:147], v[128:131], v[112:127]
	ds_read_b64_tr_b16 v[194:195], v177 offset:0x8200
	ds_read_b64_tr_b16 v[196:197], v177 offset:0x9200
	s_waitcnt lgkmcnt(6)
	v_mfma_f32_32x32x16_bf16 v[112:127], v[148:151], v[132:135], v[112:127]
	ds_read_b64_tr_b16 v[198:199], v177 offset:0xa200
	ds_read_b64_tr_b16 v[200:201], v177 offset:0xb200
	s_waitcnt lgkmcnt(6)
	v_mfma_f32_32x32x16_bf16 v[112:127], v[152:155], v[136:139], v[112:127]
	ds_read_b64_tr_b16 v[202:203], v177 offset:0xc200
	ds_read_b64_tr_b16 v[204:205], v177 offset:0xd200
	s_waitcnt lgkmcnt(6)
	v_mfma_f32_32x32x16_bf16 v[112:127], v[156:159], v[140:143], v[112:127]
	ds_read_b64_tr_b16 v[206:207], v177 offset:0xe200
	ds_read_b64_tr_b16 v[208:209], v177 offset:0xf200
	s_waitcnt lgkmcnt(6)
	v_mfma_f32_32x32x16_bf16 v[96:111], v[194:197], v[128:131], v[96:111]
	ds_read_b64_tr_b16 v[144:145], v177 offset:0x8400
	ds_read_b64_tr_b16 v[146:147], v177 offset:0x9400
	s_waitcnt lgkmcnt(6)
	v_mfma_f32_32x32x16_bf16 v[96:111], v[198:201], v[132:135], v[96:111]
	ds_read_b64_tr_b16 v[148:149], v177 offset:0xa400
	ds_read_b64_tr_b16 v[150:151], v177 offset:0xb400
	s_waitcnt lgkmcnt(6)
	v_mfma_f32_32x32x16_bf16 v[96:111], v[202:205], v[136:139], v[96:111]
	ds_read_b64_tr_b16 v[152:153], v177 offset:0xc400
	ds_read_b64_tr_b16 v[154:155], v177 offset:0xd400
	s_waitcnt lgkmcnt(6)
	v_mfma_f32_32x32x16_bf16 v[96:111], v[206:209], v[140:143], v[96:111]
	ds_read_b64_tr_b16 v[156:157], v177 offset:0xe400
	ds_read_b64_tr_b16 v[158:159], v177 offset:0xf400
	s_waitcnt lgkmcnt(6)
	v_mfma_f32_32x32x16_bf16 v[80:95], v[144:147], v[128:131], v[80:95]
	ds_read_b64_tr_b16 v[194:195], v177 offset:0x8600
	ds_read_b64_tr_b16 v[196:197], v177 offset:0x9600
	s_waitcnt lgkmcnt(6)
	v_mfma_f32_32x32x16_bf16 v[80:95], v[148:151], v[132:135], v[80:95]
	ds_read_b64_tr_b16 v[198:199], v177 offset:0xa600
	ds_read_b64_tr_b16 v[200:201], v177 offset:0xb600
	s_waitcnt lgkmcnt(6)
	v_mfma_f32_32x32x16_bf16 v[80:95], v[152:155], v[136:139], v[80:95]
	ds_read_b64_tr_b16 v[202:203], v177 offset:0xc600
	ds_read_b64_tr_b16 v[204:205], v177 offset:0xd600
	s_waitcnt lgkmcnt(6)
	v_mfma_f32_32x32x16_bf16 v[80:95], v[156:159], v[140:143], v[80:95]
	ds_read_b64_tr_b16 v[206:207], v177 offset:0xe600
	ds_read_b64_tr_b16 v[208:209], v177 offset:0xf600
	s_waitcnt lgkmcnt(6)
	v_mfma_f32_32x32x16_bf16 v[64:79], v[194:197], v[128:131], v[64:79]
	ds_read_b64_tr_b16 v[144:145], v177 offset:0x8800
	ds_read_b64_tr_b16 v[146:147], v177 offset:0x9800
	s_waitcnt lgkmcnt(6)
	v_mfma_f32_32x32x16_bf16 v[64:79], v[198:201], v[132:135], v[64:79]
	ds_read_b64_tr_b16 v[148:149], v177 offset:0xa800
	ds_read_b64_tr_b16 v[150:151], v177 offset:0xb800
	s_waitcnt lgkmcnt(6)
	v_mfma_f32_32x32x16_bf16 v[64:79], v[202:205], v[136:139], v[64:79]
	ds_read_b64_tr_b16 v[152:153], v177 offset:0xc800
	ds_read_b64_tr_b16 v[154:155], v177 offset:0xd800
	s_waitcnt lgkmcnt(6)
	v_mfma_f32_32x32x16_bf16 v[64:79], v[206:209], v[140:143], v[64:79]
	ds_read_b64_tr_b16 v[156:157], v177 offset:0xe800
	ds_read_b64_tr_b16 v[158:159], v177 offset:0xf800
	s_waitcnt lgkmcnt(6)
	v_mfma_f32_32x32x16_bf16 v[48:63], v[144:147], v[128:131], v[48:63]
	ds_read_b64_tr_b16 v[194:195], v177 offset:0x8a00
	ds_read_b64_tr_b16 v[196:197], v177 offset:0x9a00
	s_waitcnt lgkmcnt(6)
	v_mfma_f32_32x32x16_bf16 v[48:63], v[148:151], v[132:135], v[48:63]
	ds_read_b64_tr_b16 v[198:199], v177 offset:0xaa00
	ds_read_b64_tr_b16 v[200:201], v177 offset:0xba00
	s_waitcnt lgkmcnt(6)
	v_mfma_f32_32x32x16_bf16 v[48:63], v[152:155], v[136:139], v[48:63]
	ds_read_b64_tr_b16 v[202:203], v177 offset:0xca00
	ds_read_b64_tr_b16 v[204:205], v177 offset:0xda00
	s_waitcnt lgkmcnt(6)
	v_mfma_f32_32x32x16_bf16 v[48:63], v[156:159], v[140:143], v[48:63]
	ds_read_b64_tr_b16 v[206:207], v177 offset:0xea00
	ds_read_b64_tr_b16 v[208:209], v177 offset:0xfa00
	s_waitcnt lgkmcnt(6)
	v_mfma_f32_32x32x16_bf16 v[32:47], v[194:197], v[128:131], v[32:47]
	ds_read_b64_tr_b16 v[144:145], v177 offset:0x8c00
	ds_read_b64_tr_b16 v[146:147], v177 offset:0x9c00
	s_waitcnt lgkmcnt(6)
	v_mfma_f32_32x32x16_bf16 v[32:47], v[198:201], v[132:135], v[32:47]
	ds_read_b64_tr_b16 v[148:149], v177 offset:0xac00
	ds_read_b64_tr_b16 v[150:151], v177 offset:0xbc00
	s_waitcnt lgkmcnt(6)
	v_mfma_f32_32x32x16_bf16 v[32:47], v[202:205], v[136:139], v[32:47]
	ds_read_b64_tr_b16 v[152:153], v177 offset:0xcc00
	ds_read_b64_tr_b16 v[154:155], v177 offset:0xdc00
	s_waitcnt lgkmcnt(6)
	v_mfma_f32_32x32x16_bf16 v[32:47], v[206:209], v[140:143], v[32:47]
	ds_read_b64_tr_b16 v[156:157], v177 offset:0xec00
	ds_read_b64_tr_b16 v[158:159], v177 offset:0xfc00
	s_waitcnt lgkmcnt(6)
	v_mfma_f32_32x32x16_bf16 v[16:31], v[144:147], v[128:131], v[16:31]
	ds_read_b64_tr_b16 v[194:195], v177 offset:0x8e00
	ds_read_b64_tr_b16 v[196:197], v177 offset:0x9e00
	s_waitcnt lgkmcnt(6)
	v_mfma_f32_32x32x16_bf16 v[16:31], v[148:151], v[132:135], v[16:31]
	ds_read_b64_tr_b16 v[198:199], v177 offset:0xae00
	ds_read_b64_tr_b16 v[200:201], v177 offset:0xbe00
	s_waitcnt lgkmcnt(6)
	v_mfma_f32_32x32x16_bf16 v[16:31], v[152:155], v[136:139], v[16:31]
	ds_read_b64_tr_b16 v[202:203], v177 offset:0xce00
	ds_read_b64_tr_b16 v[204:205], v177 offset:0xde00
	s_waitcnt lgkmcnt(6)
	v_mfma_f32_32x32x16_bf16 v[16:31], v[156:159], v[140:143], v[16:31]
	ds_read_b64_tr_b16 v[206:207], v177 offset:0xee00
	ds_read_b64_tr_b16 v[208:209], v177 offset:0xfe00
	s_waitcnt lgkmcnt(6)
	v_mfma_f32_32x32x16_bf16 v[0:15], v[194:197], v[128:131], v[0:15]
	ds_read_b128 v[236:239], v181 offset:0
	ds_read_b128 v[240:243], v181 offset:0x2000
	s_waitcnt lgkmcnt(6)
	v_mfma_f32_32x32x16_bf16 v[0:15], v[198:201], v[132:135], v[0:15]
	ds_read_b128 v[244:247], v180 offset:0
	ds_read_b128 v[248:251], v182 offset:0
	s_waitcnt lgkmcnt(6)
	v_mfma_f32_32x32x16_bf16 v[0:15], v[202:205], v[136:139], v[0:15]
	ds_read_b128 v[218:221], v182 offset:0x2000
	ds_read_b128 v[222:225], v180 offset:0x400
	s_waitcnt lgkmcnt(6)
	v_mfma_f32_32x32x16_bf16 v[0:15], v[206:209], v[140:143], v[0:15]
	s_waitcnt lgkmcnt(3)
	s_nop 0
	v_mfma_f32_32x32x16_bf16 v[144:159], v[236:239], v[244:247], 0
	ds_read_b128 v[194:197], v183 offset:0
	ds_read_b128 v[198:201], v183 offset:0x2000
	v_mfma_f32_32x32x16_bf16 v[128:143], v[240:243], v[244:247], 0
	ds_read_b128 v[202:205], v180 offset:0x800
	s_waitcnt lgkmcnt(3)
	v_mfma_f32_32x32x16_bf16 v[144:159], v[248:251], v[222:225], v[144:159]
	ds_read_b128 v[236:239], v184 offset:0
	ds_read_b128 v[240:243], v184 offset:0x2000
	v_mfma_f32_32x32x16_bf16 v[128:143], v[218:221], v[222:225], v[128:143]
	ds_read_b128 v[244:247], v180 offset:0xc00
	s_waitcnt lgkmcnt(3)
	v_mfma_f32_32x32x16_bf16 v[144:159], v[194:197], v[202:205], v[144:159]
	ds_read_b128 v[248:251], v181 offset:0x80
	ds_read_b128 v[218:221], v181 offset:0x2080
	v_mfma_f32_32x32x16_bf16 v[128:143], v[198:201], v[202:205], v[128:143]
	ds_read_b128 v[222:225], v180 offset:0x1000
	s_waitcnt lgkmcnt(3)
	v_mfma_f32_32x32x16_bf16 v[144:159], v[236:239], v[244:247], v[144:159]
	ds_read_b128 v[194:197], v182 offset:0x80
	ds_read_b128 v[198:201], v182 offset:0x2080
	v_mfma_f32_32x32x16_bf16 v[128:143], v[240:243], v[244:247], v[128:143]
	ds_read_b128 v[202:205], v180 offset:0x1400
	s_waitcnt lgkmcnt(3)
	v_mfma_f32_32x32x16_bf16 v[144:159], v[248:251], v[222:225], v[144:159]
	ds_read_b128 v[236:239], v183 offset:0x80
	ds_read_b128 v[240:243], v183 offset:0x2080
	v_mfma_f32_32x32x16_bf16 v[128:143], v[218:221], v[222:225], v[128:143]
	ds_read_b128 v[244:247], v180 offset:0x1800
	s_waitcnt lgkmcnt(3)
	v_mfma_f32_32x32x16_bf16 v[144:159], v[194:197], v[202:205], v[144:159]
	ds_read_b128 v[248:251], v184 offset:0x80
	ds_read_b128 v[218:221], v184 offset:0x2080
	v_mfma_f32_32x32x16_bf16 v[128:143], v[198:201], v[202:205], v[128:143]
	s_waitcnt lgkmcnt(2)
	v_mfma_f32_32x32x16_bf16 v[144:159], v[236:239], v[244:247], v[144:159]
	v_mfma_f32_32x32x16_bf16 v[128:143], v[240:243], v[244:247], v[128:143]
	s_waitcnt lgkmcnt(0)
	v_mfma_f32_32x32x16_bf16 v[144:159], v[248:251], v[166:169], v[144:159]
	v_mfma_f32_32x32x16_bf16 v[128:143], v[218:221], v[166:169], v[128:143]
	s_bitcmp0_b32 s100, 8
	s_cbranch_scc1 .Lstg_a19
	s_waitcnt vmcnt(0)
	s_waitcnt lgkmcnt(0)
	s_barrier
	s_sleep 5

.LBB0_612:
	ds_read_b64_tr_b16 v[144:145], v177 offset:0
	ds_read_b64_tr_b16 v[146:147], v177 offset:0x1000
	ds_read_b64_tr_b16 v[148:149], v177 offset:0x2000
	ds_read_b64_tr_b16 v[150:151], v177 offset:0x3000
	ds_read_b64_tr_b16 v[152:153], v177 offset:0x4000
	ds_read_b64_tr_b16 v[154:155], v177 offset:0x5000
	ds_read_b64_tr_b16 v[156:157], v177 offset:0x6000
	ds_read_b64_tr_b16 v[158:159], v177 offset:0x7000
	s_waitcnt lgkmcnt(6)
	s_nop 0
	v_mfma_f32_32x32x16_bf16 v[112:127], v[144:147], v[128:131], v[112:127]
	ds_read_b64_tr_b16 v[192:193], v177 offset:0x200
	ds_read_b64_tr_b16 v[194:195], v177 offset:0x1200
	s_waitcnt lgkmcnt(6)
	v_mfma_f32_32x32x16_bf16 v[112:127], v[148:151], v[132:135], v[112:127]
	ds_read_b64_tr_b16 v[196:197], v177 offset:0x2200
	ds_read_b64_tr_b16 v[198:199], v177 offset:0x3200
	s_waitcnt lgkmcnt(6)
	v_mfma_f32_32x32x16_bf16 v[112:127], v[152:155], v[136:139], v[112:127]
	ds_read_b64_tr_b16 v[200:201], v177 offset:0x4200
	ds_read_b64_tr_b16 v[202:203], v177 offset:0x5200
	s_waitcnt lgkmcnt(6)
	v_mfma_f32_32x32x16_bf16 v[112:127], v[156:159], v[140:143], v[112:127]
	ds_read_b64_tr_b16 v[204:205], v177 offset:0x6200
	ds_read_b64_tr_b16 v[206:207], v177 offset:0x7200
	s_waitcnt lgkmcnt(6)
	v_mfma_f32_32x32x16_bf16 v[96:111], v[192:195], v[128:131], v[96:111]
	ds_read_b64_tr_b16 v[144:145], v177 offset:0x400
	ds_read_b64_tr_b16 v[146:147], v177 offset:0x1400
	s_waitcnt lgkmcnt(6)
	v_mfma_f32_32x32x16_bf16 v[96:111], v[196:199], v[132:135], v[96:111]
	ds_read_b64_tr_b16 v[148:149], v177 offset:0x2400
	ds_read_b64_tr_b16 v[150:151], v177 offset:0x3400
	s_waitcnt lgkmcnt(6)
	v_mfma_f32_32x32x16_bf16 v[96:111], v[200:203], v[136:139], v[96:111]
	ds_read_b64_tr_b16 v[152:153], v177 offset:0x4400
	ds_read_b64_tr_b16 v[154:155], v177 offset:0x5400
	s_waitcnt lgkmcnt(6)
	v_mfma_f32_32x32x16_bf16 v[96:111], v[204:207], v[140:143], v[96:111]
	ds_read_b64_tr_b16 v[156:157], v177 offset:0x6400
	ds_read_b64_tr_b16 v[158:159], v177 offset:0x7400
	s_waitcnt lgkmcnt(6)
	v_mfma_f32_32x32x16_bf16 v[80:95], v[144:147], v[128:131], v[80:95]
	ds_read_b64_tr_b16 v[192:193], v177 offset:0x600
	ds_read_b64_tr_b16 v[194:195], v177 offset:0x1600
	s_waitcnt lgkmcnt(6)
	v_mfma_f32_32x32x16_bf16 v[80:95], v[148:151], v[132:135], v[80:95]
	ds_read_b64_tr_b16 v[196:197], v177 offset:0x2600
	ds_read_b64_tr_b16 v[198:199], v177 offset:0x3600
	s_waitcnt lgkmcnt(6)
	v_mfma_f32_32x32x16_bf16 v[80:95], v[152:155], v[136:139], v[80:95]
	ds_read_b64_tr_b16 v[200:201], v177 offset:0x4600
	ds_read_b64_tr_b16 v[202:203], v177 offset:0x5600
	s_waitcnt lgkmcnt(6)
	v_mfma_f32_32x32x16_bf16 v[80:95], v[156:159], v[140:143], v[80:95]
	ds_read_b64_tr_b16 v[204:205], v177 offset:0x6600
	ds_read_b64_tr_b16 v[206:207], v177 offset:0x7600
	s_waitcnt lgkmcnt(6)
	v_mfma_f32_32x32x16_bf16 v[64:79], v[192:195], v[128:131], v[64:79]
	ds_read_b64_tr_b16 v[144:145], v177 offset:0x800
	ds_read_b64_tr_b16 v[146:147], v177 offset:0x1800
	s_waitcnt lgkmcnt(6)
	v_mfma_f32_32x32x16_bf16 v[64:79], v[196:199], v[132:135], v[64:79]
	ds_read_b64_tr_b16 v[148:149], v177 offset:0x2800
	ds_read_b64_tr_b16 v[150:151], v177 offset:0x3800
	s_waitcnt lgkmcnt(6)
	v_mfma_f32_32x32x16_bf16 v[64:79], v[200:203], v[136:139], v[64:79]
	ds_read_b64_tr_b16 v[152:153], v177 offset:0x4800
	ds_read_b64_tr_b16 v[154:155], v177 offset:0x5800
	s_waitcnt lgkmcnt(6)
	v_mfma_f32_32x32x16_bf16 v[64:79], v[204:207], v[140:143], v[64:79]
	ds_read_b64_tr_b16 v[156:157], v177 offset:0x6800
	ds_read_b64_tr_b16 v[158:159], v177 offset:0x7800
	s_waitcnt lgkmcnt(6)
	v_mfma_f32_32x32x16_bf16 v[48:63], v[144:147], v[128:131], v[48:63]
	ds_read_b64_tr_b16 v[192:193], v177 offset:0xa00
	ds_read_b64_tr_b16 v[194:195], v177 offset:0x1a00
	s_waitcnt lgkmcnt(6)
	v_mfma_f32_32x32x16_bf16 v[48:63], v[148:151], v[132:135], v[48:63]
	ds_read_b64_tr_b16 v[196:197], v177 offset:0x2a00
	ds_read_b64_tr_b16 v[198:199], v177 offset:0x3a00
	s_waitcnt lgkmcnt(6)
	v_mfma_f32_32x32x16_bf16 v[48:63], v[152:155], v[136:139], v[48:63]
	ds_read_b64_tr_b16 v[200:201], v177 offset:0x4a00
	ds_read_b64_tr_b16 v[202:203], v177 offset:0x5a00
	s_waitcnt lgkmcnt(6)
	v_mfma_f32_32x32x16_bf16 v[48:63], v[156:159], v[140:143], v[48:63]
	ds_read_b64_tr_b16 v[204:205], v177 offset:0x6a00
	ds_read_b64_tr_b16 v[206:207], v177 offset:0x7a00
	s_waitcnt lgkmcnt(6)
	v_mfma_f32_32x32x16_bf16 v[32:47], v[192:195], v[128:131], v[32:47]
	ds_read_b64_tr_b16 v[144:145], v177 offset:0xc00
	ds_read_b64_tr_b16 v[146:147], v177 offset:0x1c00
	s_waitcnt lgkmcnt(6)
	v_mfma_f32_32x32x16_bf16 v[32:47], v[196:199], v[132:135], v[32:47]
	ds_read_b64_tr_b16 v[148:149], v177 offset:0x2c00
	ds_read_b64_tr_b16 v[150:151], v177 offset:0x3c00
	s_waitcnt lgkmcnt(6)
	v_mfma_f32_32x32x16_bf16 v[32:47], v[200:203], v[136:139], v[32:47]
	ds_read_b64_tr_b16 v[152:153], v177 offset:0x4c00
	ds_read_b64_tr_b16 v[154:155], v177 offset:0x5c00
	s_waitcnt lgkmcnt(6)
	v_mfma_f32_32x32x16_bf16 v[32:47], v[204:207], v[140:143], v[32:47]
	ds_read_b64_tr_b16 v[156:157], v177 offset:0x6c00
	ds_read_b64_tr_b16 v[158:159], v177 offset:0x7c00
	s_waitcnt lgkmcnt(6)
	v_mfma_f32_32x32x16_bf16 v[16:31], v[144:147], v[128:131], v[16:31]
	ds_read_b64_tr_b16 v[192:193], v177 offset:0xe00
	ds_read_b64_tr_b16 v[194:195], v177 offset:0x1e00
	s_waitcnt lgkmcnt(6)
	v_mfma_f32_32x32x16_bf16 v[16:31], v[148:151], v[132:135], v[16:31]
	ds_read_b64_tr_b16 v[196:197], v177 offset:0x2e00
	ds_read_b64_tr_b16 v[198:199], v177 offset:0x3e00
	s_waitcnt lgkmcnt(6)
	v_mfma_f32_32x32x16_bf16 v[16:31], v[152:155], v[136:139], v[16:31]
	ds_read_b64_tr_b16 v[200:201], v177 offset:0x4e00
	ds_read_b64_tr_b16 v[202:203], v177 offset:0x5e00
	s_waitcnt lgkmcnt(6)
	v_mfma_f32_32x32x16_bf16 v[16:31], v[156:159], v[140:143], v[16:31]
	ds_read_b64_tr_b16 v[204:205], v177 offset:0x6e00
	ds_read_b64_tr_b16 v[206:207], v177 offset:0x7e00
	s_waitcnt lgkmcnt(6)
	v_mfma_f32_32x32x16_bf16 v[0:15], v[192:195], v[128:131], v[0:15]
	s_waitcnt lgkmcnt(4)
	v_mfma_f32_32x32x16_bf16 v[0:15], v[196:199], v[132:135], v[0:15]
	s_waitcnt lgkmcnt(2)
	v_mfma_f32_32x32x16_bf16 v[0:15], v[200:203], v[136:139], v[0:15]
	s_waitcnt lgkmcnt(0)
	v_mfma_f32_32x32x16_bf16 v[0:15], v[204:207], v[140:143], v[0:15]
	ds_read_b128 v[128:131], v188 offset:0
	ds_read_b128 v[132:135], v188 offset:0x2000
	ds_read_b128 v[136:139], v180 offset:0
	ds_read_b128 v[192:195], v187 offset:0
	ds_read_b128 v[196:199], v187 offset:0x2000
	ds_read_b128 v[200:203], v180 offset:0x400
	s_waitcnt lgkmcnt(3)
	s_nop 0
	v_mfma_f32_32x32x16_bf16 v[144:159], v[128:131], v[136:139], 0
	v_mfma_f32_32x32x16_bf16 v[128:143], v[132:135], v[136:139], 0
	ds_read_b128 v[204:207], v186 offset:0
	ds_read_b128 v[208:211], v186 offset:0x2000
	ds_read_b128 v[212:215], v180 offset:0x800
	s_waitcnt lgkmcnt(3)
	v_mfma_f32_32x32x16_bf16 v[144:159], v[192:195], v[200:203], v[144:159]
	v_mfma_f32_32x32x16_bf16 v[128:143], v[196:199], v[200:203], v[128:143]
	ds_read_b128 v[192:195], v185 offset:0
	ds_read_b128 v[196:199], v185 offset:0x2000
	ds_read_b128 v[200:203], v180 offset:0xc00
	s_waitcnt lgkmcnt(3)
	v_mfma_f32_32x32x16_bf16 v[144:159], v[204:207], v[212:215], v[144:159]
	v_mfma_f32_32x32x16_bf16 v[128:143], v[208:211], v[212:215], v[128:143]
	ds_read_b128 v[204:207], v188 offset:0x80
	ds_read_b128 v[208:211], v188 offset:0x2080
	ds_read_b128 v[212:215], v180 offset:0x1000
	s_waitcnt lgkmcnt(3)
	v_mfma_f32_32x32x16_bf16 v[144:159], v[192:195], v[200:203], v[144:159]
	v_mfma_f32_32x32x16_bf16 v[128:143], v[196:199], v[200:203], v[128:143]
	ds_read_b128 v[192:195], v187 offset:0x80
	ds_read_b128 v[196:199], v187 offset:0x2080
	ds_read_b128 v[200:203], v180 offset:0x1400
	s_waitcnt lgkmcnt(3)
	v_mfma_f32_32x32x16_bf16 v[144:159], v[204:207], v[212:215], v[144:159]
	v_mfma_f32_32x32x16_bf16 v[128:143], v[208:211], v[212:215], v[128:143]
	ds_read_b128 v[204:207], v186 offset:0x80
	ds_read_b128 v[208:211], v186 offset:0x2080
	ds_read_b128 v[186:189], v180 offset:0x1800
	s_waitcnt lgkmcnt(3)
	v_mfma_f32_32x32x16_bf16 v[144:159], v[192:195], v[200:203], v[144:159]
	v_mfma_f32_32x32x16_bf16 v[128:143], v[196:199], v[200:203], v[128:143]
	ds_read_b128 v[180:183], v185 offset:0x80
	ds_read_b128 v[192:195], v185 offset:0x2080
	s_waitcnt lgkmcnt(2)
	v_mfma_f32_32x32x16_bf16 v[144:159], v[204:207], v[186:189], v[144:159]
	v_mfma_f32_32x32x16_bf16 v[128:143], v[208:211], v[186:189], v[128:143]
	s_waitcnt lgkmcnt(0)
	v_mfma_f32_32x32x16_bf16 v[144:159], v[180:183], v[166:169], v[144:159]
	v_mfma_f32_32x32x16_bf16 v[128:143], v[192:195], v[166:169], v[128:143]
	s_bitcmp0_b32 s100, 8
	s_cbranch_scc1 .Lstg_a20
	s_waitcnt vmcnt(0)
	s_waitcnt lgkmcnt(0)
	s_barrier
	s_sleep 5
